# P7 fixed conversion share: 8x16 item tiles per workgroup, concurrent items 4 row blocks x 2 column blocks (512 B contiguous fp8 writes)
# speedup vs baseline: 1.0011x; 1.0010x over previous
.LBB0_993:
	s_add_u32 s38, s90, 0x4b100000
	s_addc_u32 s39, s91, 0
	v_readlane_b32 s3, v255, 4
	s_bitcmp0_b32 s3, 0
	s_cbranch_scc1 .LBB0_1024
	s_waitcnt vmcnt(0)
	v_readlane_b32 s2, v255, 28
	s_lshr_b32 s0, s3, 1
	s_lshr_b32 s1, s0, 3
	s_lshl_b32 s20, s1, 10
	s_and_b32 s0, s0, 7
	s_lshr_b32 s1, s0, 2
	s_lshl_b32 s1, s1, 3
	s_and_b32 s4, s2, 3
	s_add_i32 s1, s1, s4
	s_lshl_b32 s1, s1, 6
	s_add_i32 s20, s20, s1
	s_and_b32 s0, s0, 3
	s_lshl_b32 s0, s0, 4
	s_add_i32 s20, s20, s0
	s_lshr_b32 s4, s2, 2
	s_add_i32 s20, s20, s4
	v_mbcnt_lo_u32_b32 v210, -1, 0
	v_mbcnt_hi_u32_b32 v210, -1, v210
	v_lshrrev_b32_e32 v211, 3, v210
	v_and_b32_e32 v210, 7, v210
	v_lshlrev_b32_e32 v208, 17, v211
	v_lshl_or_b32 v208, v210, 4, v208
	v_lshlrev_b32_e32 v209, 13, v210
	v_lshl_or_b32 v209, v211, 4, v209
	s_mov_b32 s16, 0x44000000
	s_add_i32 s1, s20, 0
	s_lshr_b32 s2, s1, 10
	s_and_b32 s4, s1, 0x3ff
	s_lshr_b32 s5, s4, 6
	s_and_b32 s4, s4, 63
	s_lshl_b32 s12, s2, 24
	s_lshl_b32 s13, s5, 20
	s_add_i32 s12, s12, s13
	s_lshl_b32 s13, s4, 7
	s_add_i32 s12, s12, s13
	s_add_u32 s14, s70, s12
	s_addc_u32 s15, s71, 0
	global_load_dwordx4 v[0:3], v208, s[14:15] sc1 nt
	s_add_u32 s18, s14, 0x2000
	s_addc_u32 s19, s15, 0
	global_load_dwordx4 v[4:7], v208, s[18:19] sc1 nt
	s_add_u32 s18, s14, 0x4000
	s_addc_u32 s19, s15, 0
	global_load_dwordx4 v[8:11], v208, s[18:19] sc1 nt
	s_add_u32 s18, s14, 0x6000
	s_addc_u32 s19, s15, 0
	global_load_dwordx4 v[12:15], v208, s[18:19] sc1 nt
	s_add_u32 s18, s14, 0x8000
	s_addc_u32 s19, s15, 0
	global_load_dwordx4 v[16:19], v208, s[18:19] sc1 nt
	s_add_u32 s18, s14, 0xa000
	s_addc_u32 s19, s15, 0
	global_load_dwordx4 v[20:23], v208, s[18:19] sc1 nt
	s_add_u32 s18, s14, 0xc000
	s_addc_u32 s19, s15, 0
	global_load_dwordx4 v[24:27], v208, s[18:19] sc1 nt
	s_add_u32 s18, s14, 0xe000
	s_addc_u32 s19, s15, 0
	global_load_dwordx4 v[28:31], v208, s[18:19] sc1 nt
	s_add_u32 s18, s14, 0x10000
	s_addc_u32 s19, s15, 0
	global_load_dwordx4 v[32:35], v208, s[18:19] sc1 nt
	s_add_u32 s18, s14, 0x12000
	s_addc_u32 s19, s15, 0
	global_load_dwordx4 v[36:39], v208, s[18:19] sc1 nt
	s_add_u32 s18, s14, 0x14000
	s_addc_u32 s19, s15, 0
	global_load_dwordx4 v[40:43], v208, s[18:19] sc1 nt
	s_add_u32 s18, s14, 0x16000
	s_addc_u32 s19, s15, 0
	global_load_dwordx4 v[44:47], v208, s[18:19] sc1 nt
	s_add_u32 s18, s14, 0x18000
	s_addc_u32 s19, s15, 0
	global_load_dwordx4 v[48:51], v208, s[18:19] sc1 nt
	s_add_u32 s18, s14, 0x1a000
	s_addc_u32 s19, s15, 0
	global_load_dwordx4 v[52:55], v208, s[18:19] sc1 nt
	s_add_u32 s18, s14, 0x1c000
	s_addc_u32 s19, s15, 0
	global_load_dwordx4 v[56:59], v208, s[18:19] sc1 nt
	s_add_u32 s18, s14, 0x1e000
	s_addc_u32 s19, s15, 0
	global_load_dwordx4 v[60:63], v208, s[18:19] sc1 nt
	s_add_i32 s1, s20, 256
	s_lshr_b32 s2, s1, 10
	s_and_b32 s4, s1, 0x3ff
	s_lshr_b32 s5, s4, 6
	s_and_b32 s4, s4, 63
	s_lshl_b32 s12, s2, 24
	s_lshl_b32 s13, s5, 20
	s_add_i32 s12, s12, s13
	s_lshl_b32 s13, s4, 7
	s_add_i32 s12, s12, s13
	s_add_u32 s14, s70, s12
	s_addc_u32 s15, s71, 0
	global_load_dwordx4 v[64:67], v208, s[14:15] sc1 nt
	s_add_u32 s18, s14, 0x2000
	s_addc_u32 s19, s15, 0
	global_load_dwordx4 v[68:71], v208, s[18:19] sc1 nt
	s_add_u32 s18, s14, 0x4000
	s_addc_u32 s19, s15, 0
	global_load_dwordx4 v[72:75], v208, s[18:19] sc1 nt
	s_add_u32 s18, s14, 0x6000
	s_addc_u32 s19, s15, 0
	global_load_dwordx4 v[76:79], v208, s[18:19] sc1 nt
	s_add_u32 s18, s14, 0x8000
	s_addc_u32 s19, s15, 0
	global_load_dwordx4 v[80:83], v208, s[18:19] sc1 nt
	s_add_u32 s18, s14, 0xa000
	s_addc_u32 s19, s15, 0
	global_load_dwordx4 v[84:87], v208, s[18:19] sc1 nt
	s_add_u32 s18, s14, 0xc000
	s_addc_u32 s19, s15, 0
	global_load_dwordx4 v[88:91], v208, s[18:19] sc1 nt
	s_add_u32 s18, s14, 0xe000
	s_addc_u32 s19, s15, 0
	global_load_dwordx4 v[92:95], v208, s[18:19] sc1 nt
	s_add_u32 s18, s14, 0x10000
	s_addc_u32 s19, s15, 0
	global_load_dwordx4 v[96:99], v208, s[18:19] sc1 nt
	s_add_u32 s18, s14, 0x12000
	s_addc_u32 s19, s15, 0
	global_load_dwordx4 v[100:103], v208, s[18:19] sc1 nt
	s_add_u32 s18, s14, 0x14000
	s_addc_u32 s19, s15, 0
	global_load_dwordx4 v[104:107], v208, s[18:19] sc1 nt
	s_add_u32 s18, s14, 0x16000
	s_addc_u32 s19, s15, 0
	global_load_dwordx4 v[108:111], v208, s[18:19] sc1 nt
	s_add_u32 s18, s14, 0x18000
	s_addc_u32 s19, s15, 0
	global_load_dwordx4 v[112:115], v208, s[18:19] sc1 nt
	s_add_u32 s18, s14, 0x1a000
	s_addc_u32 s19, s15, 0
	global_load_dwordx4 v[116:119], v208, s[18:19] sc1 nt
	s_add_u32 s18, s14, 0x1c000
	s_addc_u32 s19, s15, 0
	global_load_dwordx4 v[120:123], v208, s[18:19] sc1 nt
	s_add_u32 s18, s14, 0x1e000
	s_addc_u32 s19, s15, 0
	global_load_dwordx4 v[124:127], v208, s[18:19] sc1 nt
	s_add_i32 s1, s20, 2
	s_lshr_b32 s2, s1, 10
	s_and_b32 s4, s1, 0x3ff
	s_lshr_b32 s5, s4, 6
	s_and_b32 s4, s4, 63
	s_lshl_b32 s12, s2, 24
	s_lshl_b32 s13, s5, 20
	s_add_i32 s12, s12, s13
	s_lshl_b32 s13, s4, 7
	s_add_i32 s12, s12, s13
	s_add_u32 s14, s70, s12
	s_addc_u32 s15, s71, 0
	global_load_dwordx4 v[128:131], v208, s[14:15] sc1 nt
	s_add_u32 s18, s14, 0x2000
	s_addc_u32 s19, s15, 0
	global_load_dwordx4 v[132:135], v208, s[18:19] sc1 nt
	s_add_u32 s18, s14, 0x4000
	s_addc_u32 s19, s15, 0
	global_load_dwordx4 v[136:139], v208, s[18:19] sc1 nt
	s_add_u32 s18, s14, 0x6000
	s_addc_u32 s19, s15, 0
	global_load_dwordx4 v[140:143], v208, s[18:19] sc1 nt
	s_add_u32 s18, s14, 0x8000
	s_addc_u32 s19, s15, 0
	global_load_dwordx4 v[144:147], v208, s[18:19] sc1 nt
	s_add_u32 s18, s14, 0xa000
	s_addc_u32 s19, s15, 0
	global_load_dwordx4 v[148:151], v208, s[18:19] sc1 nt
	s_add_u32 s18, s14, 0xc000
	s_addc_u32 s19, s15, 0
	global_load_dwordx4 v[152:155], v208, s[18:19] sc1 nt
	s_add_u32 s18, s14, 0xe000
	s_addc_u32 s19, s15, 0
	global_load_dwordx4 v[156:159], v208, s[18:19] sc1 nt
	s_add_u32 s18, s14, 0x10000
	s_addc_u32 s19, s15, 0
	global_load_dwordx4 v[160:163], v208, s[18:19] sc1 nt
	s_add_u32 s18, s14, 0x12000
	s_addc_u32 s19, s15, 0
	global_load_dwordx4 v[164:167], v208, s[18:19] sc1 nt
	s_add_u32 s18, s14, 0x14000
	s_addc_u32 s19, s15, 0
	global_load_dwordx4 v[168:171], v208, s[18:19] sc1 nt
	s_add_u32 s18, s14, 0x16000
	s_addc_u32 s19, s15, 0
	global_load_dwordx4 v[172:175], v208, s[18:19] sc1 nt
	s_add_u32 s18, s14, 0x18000
	s_addc_u32 s19, s15, 0
	global_load_dwordx4 v[176:179], v208, s[18:19] sc1 nt
	s_add_u32 s18, s14, 0x1a000
	s_addc_u32 s19, s15, 0
	global_load_dwordx4 v[180:183], v208, s[18:19] sc1 nt
	s_add_u32 s18, s14, 0x1c000
	s_addc_u32 s19, s15, 0
	global_load_dwordx4 v[184:187], v208, s[18:19] sc1 nt
	s_add_u32 s18, s14, 0x1e000
	s_addc_u32 s19, s15, 0
	global_load_dwordx4 v[188:191], v208, s[18:19] sc1 nt
	s_waitcnt vmcnt(32)
	s_add_i32 s1, s20, 0
	s_lshr_b32 s2, s1, 10
	s_and_b32 s4, s1, 0x3ff
	s_lshr_b32 s5, s4, 6
	s_and_b32 s4, s4, 63
	s_lshl_b32 s12, s2, 22
	s_lshl_b32 s13, s4, 16
	s_add_i32 s12, s12, s13
	s_lshl_b32 s13, s5, 7
	s_add_i32 s12, s12, s13
	s_add_u32 s24, s90, s12
	s_addc_u32 s25, s91, 0
	s_add_u32 s24, s24, 0x3b100000
	s_addc_u32 s25, s25, 0
	s_add_u32 s26, s24, 0x1000
	s_addc_u32 s27, s25, 0
	v_pk_mul_f32 v[0:1], v[0:1], s[16:17] op_sel_hi:[1,0]
	v_pk_mul_f32 v[2:3], v[2:3], s[16:17] op_sel_hi:[1,0]
	v_pk_mul_f32 v[4:5], v[4:5], s[16:17] op_sel_hi:[1,0]
	v_pk_mul_f32 v[6:7], v[6:7], s[16:17] op_sel_hi:[1,0]
	v_pk_mul_f32 v[8:9], v[8:9], s[16:17] op_sel_hi:[1,0]
	v_pk_mul_f32 v[10:11], v[10:11], s[16:17] op_sel_hi:[1,0]
	v_pk_mul_f32 v[12:13], v[12:13], s[16:17] op_sel_hi:[1,0]
	v_pk_mul_f32 v[14:15], v[14:15], s[16:17] op_sel_hi:[1,0]
	v_pk_mul_f32 v[16:17], v[16:17], s[16:17] op_sel_hi:[1,0]
	v_pk_mul_f32 v[18:19], v[18:19], s[16:17] op_sel_hi:[1,0]
	v_pk_mul_f32 v[20:21], v[20:21], s[16:17] op_sel_hi:[1,0]
	v_pk_mul_f32 v[22:23], v[22:23], s[16:17] op_sel_hi:[1,0]
	v_pk_mul_f32 v[24:25], v[24:25], s[16:17] op_sel_hi:[1,0]
	v_pk_mul_f32 v[26:27], v[26:27], s[16:17] op_sel_hi:[1,0]
	v_pk_mul_f32 v[28:29], v[28:29], s[16:17] op_sel_hi:[1,0]
	v_pk_mul_f32 v[30:31], v[30:31], s[16:17] op_sel_hi:[1,0]
	v_pk_mul_f32 v[32:33], v[32:33], s[16:17] op_sel_hi:[1,0]
	v_pk_mul_f32 v[34:35], v[34:35], s[16:17] op_sel_hi:[1,0]
	v_pk_mul_f32 v[36:37], v[36:37], s[16:17] op_sel_hi:[1,0]
	v_pk_mul_f32 v[38:39], v[38:39], s[16:17] op_sel_hi:[1,0]
	v_pk_mul_f32 v[40:41], v[40:41], s[16:17] op_sel_hi:[1,0]
	v_pk_mul_f32 v[42:43], v[42:43], s[16:17] op_sel_hi:[1,0]
	v_pk_mul_f32 v[44:45], v[44:45], s[16:17] op_sel_hi:[1,0]
	v_pk_mul_f32 v[46:47], v[46:47], s[16:17] op_sel_hi:[1,0]
	v_pk_mul_f32 v[48:49], v[48:49], s[16:17] op_sel_hi:[1,0]
	v_pk_mul_f32 v[50:51], v[50:51], s[16:17] op_sel_hi:[1,0]
	v_pk_mul_f32 v[52:53], v[52:53], s[16:17] op_sel_hi:[1,0]
	v_pk_mul_f32 v[54:55], v[54:55], s[16:17] op_sel_hi:[1,0]
	v_pk_mul_f32 v[56:57], v[56:57], s[16:17] op_sel_hi:[1,0]
	v_pk_mul_f32 v[58:59], v[58:59], s[16:17] op_sel_hi:[1,0]
	v_pk_mul_f32 v[60:61], v[60:61], s[16:17] op_sel_hi:[1,0]
	v_pk_mul_f32 v[62:63], v[62:63], s[16:17] op_sel_hi:[1,0]
	v_cvt_pk_fp8_f32 v192, v0, v4
	v_cvt_pk_fp8_f32 v192, v8, v12 op_sel:[0,0,1]
	v_cvt_pk_fp8_f32 v193, v16, v20
	v_cvt_pk_fp8_f32 v193, v24, v28 op_sel:[0,0,1]
	v_cvt_pk_fp8_f32 v194, v32, v36
	v_cvt_pk_fp8_f32 v194, v40, v44 op_sel:[0,0,1]
	v_cvt_pk_fp8_f32 v195, v48, v52
	v_cvt_pk_fp8_f32 v195, v56, v60 op_sel:[0,0,1]
	global_store_dwordx4 v209, v[192:195], s[24:25] sc1
	v_cvt_pk_fp8_f32 v196, v1, v5
	v_cvt_pk_fp8_f32 v196, v9, v13 op_sel:[0,0,1]
	v_cvt_pk_fp8_f32 v197, v17, v21
	v_cvt_pk_fp8_f32 v197, v25, v29 op_sel:[0,0,1]
	v_cvt_pk_fp8_f32 v198, v33, v37
	v_cvt_pk_fp8_f32 v198, v41, v45 op_sel:[0,0,1]
	v_cvt_pk_fp8_f32 v199, v49, v53
	v_cvt_pk_fp8_f32 v199, v57, v61 op_sel:[0,0,1]
	global_store_dwordx4 v209, v[196:199], s[24:25] offset:2048 sc1
	v_cvt_pk_fp8_f32 v200, v2, v6
	v_cvt_pk_fp8_f32 v200, v10, v14 op_sel:[0,0,1]
	v_cvt_pk_fp8_f32 v201, v18, v22
	v_cvt_pk_fp8_f32 v201, v26, v30 op_sel:[0,0,1]
	v_cvt_pk_fp8_f32 v202, v34, v38
	v_cvt_pk_fp8_f32 v202, v42, v46 op_sel:[0,0,1]
	v_cvt_pk_fp8_f32 v203, v50, v54
	v_cvt_pk_fp8_f32 v203, v58, v62 op_sel:[0,0,1]
	global_store_dwordx4 v209, v[200:203], s[26:27] sc1
	v_cvt_pk_fp8_f32 v204, v3, v7
	v_cvt_pk_fp8_f32 v204, v11, v15 op_sel:[0,0,1]
	v_cvt_pk_fp8_f32 v205, v19, v23
	v_cvt_pk_fp8_f32 v205, v27, v31 op_sel:[0,0,1]
	v_cvt_pk_fp8_f32 v206, v35, v39
	v_cvt_pk_fp8_f32 v206, v43, v47 op_sel:[0,0,1]
	v_cvt_pk_fp8_f32 v207, v51, v55
	v_cvt_pk_fp8_f32 v207, v59, v63 op_sel:[0,0,1]
	global_store_dwordx4 v209, v[204:207], s[26:27] offset:2048 sc1
	s_add_i32 s1, s20, 258
	s_lshr_b32 s2, s1, 10
	s_and_b32 s4, s1, 0x3ff
	s_lshr_b32 s5, s4, 6
	s_and_b32 s4, s4, 63
	s_lshl_b32 s12, s2, 24
	s_lshl_b32 s13, s5, 20
	s_add_i32 s12, s12, s13
	s_lshl_b32 s13, s4, 7
	s_add_i32 s12, s12, s13
	s_add_u32 s14, s70, s12
	s_addc_u32 s15, s71, 0
	global_load_dwordx4 v[0:3], v208, s[14:15] sc1 nt
	s_add_u32 s18, s14, 0x2000
	s_addc_u32 s19, s15, 0
	global_load_dwordx4 v[4:7], v208, s[18:19] sc1 nt
	s_add_u32 s18, s14, 0x4000
	s_addc_u32 s19, s15, 0
	global_load_dwordx4 v[8:11], v208, s[18:19] sc1 nt
	s_add_u32 s18, s14, 0x6000
	s_addc_u32 s19, s15, 0
	global_load_dwordx4 v[12:15], v208, s[18:19] sc1 nt
	s_add_u32 s18, s14, 0x8000
	s_addc_u32 s19, s15, 0
	global_load_dwordx4 v[16:19], v208, s[18:19] sc1 nt
	s_add_u32 s18, s14, 0xa000
	s_addc_u32 s19, s15, 0
	global_load_dwordx4 v[20:23], v208, s[18:19] sc1 nt
	s_add_u32 s18, s14, 0xc000
	s_addc_u32 s19, s15, 0
	global_load_dwordx4 v[24:27], v208, s[18:19] sc1 nt
	s_add_u32 s18, s14, 0xe000
	s_addc_u32 s19, s15, 0
	global_load_dwordx4 v[28:31], v208, s[18:19] sc1 nt
	s_add_u32 s18, s14, 0x10000
	s_addc_u32 s19, s15, 0
	global_load_dwordx4 v[32:35], v208, s[18:19] sc1 nt
	s_add_u32 s18, s14, 0x12000
	s_addc_u32 s19, s15, 0
	global_load_dwordx4 v[36:39], v208, s[18:19] sc1 nt
	s_add_u32 s18, s14, 0x14000
	s_addc_u32 s19, s15, 0
	global_load_dwordx4 v[40:43], v208, s[18:19] sc1 nt
	s_add_u32 s18, s14, 0x16000
	s_addc_u32 s19, s15, 0
	global_load_dwordx4 v[44:47], v208, s[18:19] sc1 nt
	s_add_u32 s18, s14, 0x18000
	s_addc_u32 s19, s15, 0
	global_load_dwordx4 v[48:51], v208, s[18:19] sc1 nt
	s_add_u32 s18, s14, 0x1a000
	s_addc_u32 s19, s15, 0
	global_load_dwordx4 v[52:55], v208, s[18:19] sc1 nt
	s_add_u32 s18, s14, 0x1c000
	s_addc_u32 s19, s15, 0
	global_load_dwordx4 v[56:59], v208, s[18:19] sc1 nt
	s_add_u32 s18, s14, 0x1e000
	s_addc_u32 s19, s15, 0
	global_load_dwordx4 v[60:63], v208, s[18:19] sc1 nt
	s_waitcnt vmcnt(36)
	s_add_i32 s1, s20, 256
	s_lshr_b32 s2, s1, 10
	s_and_b32 s4, s1, 0x3ff
	s_lshr_b32 s5, s4, 6
	s_and_b32 s4, s4, 63
	s_lshl_b32 s12, s2, 22
	s_lshl_b32 s13, s4, 16
	s_add_i32 s12, s12, s13
	s_lshl_b32 s13, s5, 7
	s_add_i32 s12, s12, s13
	s_add_u32 s24, s90, s12
	s_addc_u32 s25, s91, 0
	s_add_u32 s24, s24, 0x3b100000
	s_addc_u32 s25, s25, 0
	s_add_u32 s26, s24, 0x1000
	s_addc_u32 s27, s25, 0
	v_pk_mul_f32 v[64:65], v[64:65], s[16:17] op_sel_hi:[1,0]
	v_pk_mul_f32 v[66:67], v[66:67], s[16:17] op_sel_hi:[1,0]
	v_pk_mul_f32 v[68:69], v[68:69], s[16:17] op_sel_hi:[1,0]
	v_pk_mul_f32 v[70:71], v[70:71], s[16:17] op_sel_hi:[1,0]
	v_pk_mul_f32 v[72:73], v[72:73], s[16:17] op_sel_hi:[1,0]
	v_pk_mul_f32 v[74:75], v[74:75], s[16:17] op_sel_hi:[1,0]
	v_pk_mul_f32 v[76:77], v[76:77], s[16:17] op_sel_hi:[1,0]
	v_pk_mul_f32 v[78:79], v[78:79], s[16:17] op_sel_hi:[1,0]
	v_pk_mul_f32 v[80:81], v[80:81], s[16:17] op_sel_hi:[1,0]
	v_pk_mul_f32 v[82:83], v[82:83], s[16:17] op_sel_hi:[1,0]
	v_pk_mul_f32 v[84:85], v[84:85], s[16:17] op_sel_hi:[1,0]
	v_pk_mul_f32 v[86:87], v[86:87], s[16:17] op_sel_hi:[1,0]
	v_pk_mul_f32 v[88:89], v[88:89], s[16:17] op_sel_hi:[1,0]
	v_pk_mul_f32 v[90:91], v[90:91], s[16:17] op_sel_hi:[1,0]
	v_pk_mul_f32 v[92:93], v[92:93], s[16:17] op_sel_hi:[1,0]
	v_pk_mul_f32 v[94:95], v[94:95], s[16:17] op_sel_hi:[1,0]
	v_pk_mul_f32 v[96:97], v[96:97], s[16:17] op_sel_hi:[1,0]
	v_pk_mul_f32 v[98:99], v[98:99], s[16:17] op_sel_hi:[1,0]
	v_pk_mul_f32 v[100:101], v[100:101], s[16:17] op_sel_hi:[1,0]
	v_pk_mul_f32 v[102:103], v[102:103], s[16:17] op_sel_hi:[1,0]
	v_pk_mul_f32 v[104:105], v[104:105], s[16:17] op_sel_hi:[1,0]
	v_pk_mul_f32 v[106:107], v[106:107], s[16:17] op_sel_hi:[1,0]
	v_pk_mul_f32 v[108:109], v[108:109], s[16:17] op_sel_hi:[1,0]
	v_pk_mul_f32 v[110:111], v[110:111], s[16:17] op_sel_hi:[1,0]
	v_pk_mul_f32 v[112:113], v[112:113], s[16:17] op_sel_hi:[1,0]
	v_pk_mul_f32 v[114:115], v[114:115], s[16:17] op_sel_hi:[1,0]
	v_pk_mul_f32 v[116:117], v[116:117], s[16:17] op_sel_hi:[1,0]
	v_pk_mul_f32 v[118:119], v[118:119], s[16:17] op_sel_hi:[1,0]
	v_pk_mul_f32 v[120:121], v[120:121], s[16:17] op_sel_hi:[1,0]
	v_pk_mul_f32 v[122:123], v[122:123], s[16:17] op_sel_hi:[1,0]
	v_pk_mul_f32 v[124:125], v[124:125], s[16:17] op_sel_hi:[1,0]
	v_pk_mul_f32 v[126:127], v[126:127], s[16:17] op_sel_hi:[1,0]
	v_cvt_pk_fp8_f32 v192, v64, v68
	v_cvt_pk_fp8_f32 v192, v72, v76 op_sel:[0,0,1]
	v_cvt_pk_fp8_f32 v193, v80, v84
	v_cvt_pk_fp8_f32 v193, v88, v92 op_sel:[0,0,1]
	v_cvt_pk_fp8_f32 v194, v96, v100
	v_cvt_pk_fp8_f32 v194, v104, v108 op_sel:[0,0,1]
	v_cvt_pk_fp8_f32 v195, v112, v116
	v_cvt_pk_fp8_f32 v195, v120, v124 op_sel:[0,0,1]
	global_store_dwordx4 v209, v[192:195], s[24:25] sc1
	v_cvt_pk_fp8_f32 v196, v65, v69
	v_cvt_pk_fp8_f32 v196, v73, v77 op_sel:[0,0,1]
	v_cvt_pk_fp8_f32 v197, v81, v85
	v_cvt_pk_fp8_f32 v197, v89, v93 op_sel:[0,0,1]
	v_cvt_pk_fp8_f32 v198, v97, v101
	v_cvt_pk_fp8_f32 v198, v105, v109 op_sel:[0,0,1]
	v_cvt_pk_fp8_f32 v199, v113, v117
	v_cvt_pk_fp8_f32 v199, v121, v125 op_sel:[0,0,1]
	global_store_dwordx4 v209, v[196:199], s[24:25] offset:2048 sc1
	v_cvt_pk_fp8_f32 v200, v66, v70
	v_cvt_pk_fp8_f32 v200, v74, v78 op_sel:[0,0,1]
	v_cvt_pk_fp8_f32 v201, v82, v86
	v_cvt_pk_fp8_f32 v201, v90, v94 op_sel:[0,0,1]
	v_cvt_pk_fp8_f32 v202, v98, v102
	v_cvt_pk_fp8_f32 v202, v106, v110 op_sel:[0,0,1]
	v_cvt_pk_fp8_f32 v203, v114, v118
	v_cvt_pk_fp8_f32 v203, v122, v126 op_sel:[0,0,1]
	global_store_dwordx4 v209, v[200:203], s[26:27] sc1
	v_cvt_pk_fp8_f32 v204, v67, v71
	v_cvt_pk_fp8_f32 v204, v75, v79 op_sel:[0,0,1]
	v_cvt_pk_fp8_f32 v205, v83, v87
	v_cvt_pk_fp8_f32 v205, v91, v95 op_sel:[0,0,1]
	v_cvt_pk_fp8_f32 v206, v99, v103
	v_cvt_pk_fp8_f32 v206, v107, v111 op_sel:[0,0,1]
	v_cvt_pk_fp8_f32 v207, v115, v119
	v_cvt_pk_fp8_f32 v207, v123, v127 op_sel:[0,0,1]
	global_store_dwordx4 v209, v[204:207], s[26:27] offset:2048 sc1
	s_add_i32 s1, s20, 4
	s_lshr_b32 s2, s1, 10
	s_and_b32 s4, s1, 0x3ff
	s_lshr_b32 s5, s4, 6
	s_and_b32 s4, s4, 63
	s_lshl_b32 s12, s2, 24
	s_lshl_b32 s13, s5, 20
	s_add_i32 s12, s12, s13
	s_lshl_b32 s13, s4, 7
	s_add_i32 s12, s12, s13
	s_add_u32 s14, s70, s12
	s_addc_u32 s15, s71, 0
	global_load_dwordx4 v[64:67], v208, s[14:15] sc1 nt
	s_add_u32 s18, s14, 0x2000
	s_addc_u32 s19, s15, 0
	global_load_dwordx4 v[68:71], v208, s[18:19] sc1 nt
	s_add_u32 s18, s14, 0x4000
	s_addc_u32 s19, s15, 0
	global_load_dwordx4 v[72:75], v208, s[18:19] sc1 nt
	s_add_u32 s18, s14, 0x6000
	s_addc_u32 s19, s15, 0
	global_load_dwordx4 v[76:79], v208, s[18:19] sc1 nt
	s_add_u32 s18, s14, 0x8000
	s_addc_u32 s19, s15, 0
	global_load_dwordx4 v[80:83], v208, s[18:19] sc1 nt
	s_add_u32 s18, s14, 0xa000
	s_addc_u32 s19, s15, 0
	global_load_dwordx4 v[84:87], v208, s[18:19] sc1 nt
	s_add_u32 s18, s14, 0xc000
	s_addc_u32 s19, s15, 0
	global_load_dwordx4 v[88:91], v208, s[18:19] sc1 nt
	s_add_u32 s18, s14, 0xe000
	s_addc_u32 s19, s15, 0
	global_load_dwordx4 v[92:95], v208, s[18:19] sc1 nt
	s_add_u32 s18, s14, 0x10000
	s_addc_u32 s19, s15, 0
	global_load_dwordx4 v[96:99], v208, s[18:19] sc1 nt
	s_add_u32 s18, s14, 0x12000
	s_addc_u32 s19, s15, 0
	global_load_dwordx4 v[100:103], v208, s[18:19] sc1 nt
	s_add_u32 s18, s14, 0x14000
	s_addc_u32 s19, s15, 0
	global_load_dwordx4 v[104:107], v208, s[18:19] sc1 nt
	s_add_u32 s18, s14, 0x16000
	s_addc_u32 s19, s15, 0
	global_load_dwordx4 v[108:111], v208, s[18:19] sc1 nt
	s_add_u32 s18, s14, 0x18000
	s_addc_u32 s19, s15, 0
	global_load_dwordx4 v[112:115], v208, s[18:19] sc1 nt
	s_add_u32 s18, s14, 0x1a000
	s_addc_u32 s19, s15, 0
	global_load_dwordx4 v[116:119], v208, s[18:19] sc1 nt
	s_add_u32 s18, s14, 0x1c000
	s_addc_u32 s19, s15, 0
	global_load_dwordx4 v[120:123], v208, s[18:19] sc1 nt
	s_add_u32 s18, s14, 0x1e000
	s_addc_u32 s19, s15, 0
	global_load_dwordx4 v[124:127], v208, s[18:19] sc1 nt
	s_waitcnt vmcnt(40)
	s_add_i32 s1, s20, 2
	s_lshr_b32 s2, s1, 10
	s_and_b32 s4, s1, 0x3ff
	s_lshr_b32 s5, s4, 6
	s_and_b32 s4, s4, 63
	s_lshl_b32 s12, s2, 22
	s_lshl_b32 s13, s4, 16
	s_add_i32 s12, s12, s13
	s_lshl_b32 s13, s5, 7
	s_add_i32 s12, s12, s13
	s_add_u32 s24, s90, s12
	s_addc_u32 s25, s91, 0
	s_add_u32 s24, s24, 0x3b100000
	s_addc_u32 s25, s25, 0
	s_add_u32 s26, s24, 0x1000
	s_addc_u32 s27, s25, 0
	v_pk_mul_f32 v[128:129], v[128:129], s[16:17] op_sel_hi:[1,0]
	v_pk_mul_f32 v[130:131], v[130:131], s[16:17] op_sel_hi:[1,0]
	v_pk_mul_f32 v[132:133], v[132:133], s[16:17] op_sel_hi:[1,0]
	v_pk_mul_f32 v[134:135], v[134:135], s[16:17] op_sel_hi:[1,0]
	v_pk_mul_f32 v[136:137], v[136:137], s[16:17] op_sel_hi:[1,0]
	v_pk_mul_f32 v[138:139], v[138:139], s[16:17] op_sel_hi:[1,0]
	v_pk_mul_f32 v[140:141], v[140:141], s[16:17] op_sel_hi:[1,0]
	v_pk_mul_f32 v[142:143], v[142:143], s[16:17] op_sel_hi:[1,0]
	v_pk_mul_f32 v[144:145], v[144:145], s[16:17] op_sel_hi:[1,0]
	v_pk_mul_f32 v[146:147], v[146:147], s[16:17] op_sel_hi:[1,0]
	v_pk_mul_f32 v[148:149], v[148:149], s[16:17] op_sel_hi:[1,0]
	v_pk_mul_f32 v[150:151], v[150:151], s[16:17] op_sel_hi:[1,0]
	v_pk_mul_f32 v[152:153], v[152:153], s[16:17] op_sel_hi:[1,0]
	v_pk_mul_f32 v[154:155], v[154:155], s[16:17] op_sel_hi:[1,0]
	v_pk_mul_f32 v[156:157], v[156:157], s[16:17] op_sel_hi:[1,0]
	v_pk_mul_f32 v[158:159], v[158:159], s[16:17] op_sel_hi:[1,0]
	v_pk_mul_f32 v[160:161], v[160:161], s[16:17] op_sel_hi:[1,0]
	v_pk_mul_f32 v[162:163], v[162:163], s[16:17] op_sel_hi:[1,0]
	v_pk_mul_f32 v[164:165], v[164:165], s[16:17] op_sel_hi:[1,0]
	v_pk_mul_f32 v[166:167], v[166:167], s[16:17] op_sel_hi:[1,0]
	v_pk_mul_f32 v[168:169], v[168:169], s[16:17] op_sel_hi:[1,0]
	v_pk_mul_f32 v[170:171], v[170:171], s[16:17] op_sel_hi:[1,0]
	v_pk_mul_f32 v[172:173], v[172:173], s[16:17] op_sel_hi:[1,0]
	v_pk_mul_f32 v[174:175], v[174:175], s[16:17] op_sel_hi:[1,0]
	v_pk_mul_f32 v[176:177], v[176:177], s[16:17] op_sel_hi:[1,0]
	v_pk_mul_f32 v[178:179], v[178:179], s[16:17] op_sel_hi:[1,0]
	v_pk_mul_f32 v[180:181], v[180:181], s[16:17] op_sel_hi:[1,0]
	v_pk_mul_f32 v[182:183], v[182:183], s[16:17] op_sel_hi:[1,0]
	v_pk_mul_f32 v[184:185], v[184:185], s[16:17] op_sel_hi:[1,0]
	v_pk_mul_f32 v[186:187], v[186:187], s[16:17] op_sel_hi:[1,0]
	v_pk_mul_f32 v[188:189], v[188:189], s[16:17] op_sel_hi:[1,0]
	v_pk_mul_f32 v[190:191], v[190:191], s[16:17] op_sel_hi:[1,0]
	v_cvt_pk_fp8_f32 v192, v128, v132
	v_cvt_pk_fp8_f32 v192, v136, v140 op_sel:[0,0,1]
	v_cvt_pk_fp8_f32 v193, v144, v148
	v_cvt_pk_fp8_f32 v193, v152, v156 op_sel:[0,0,1]
	v_cvt_pk_fp8_f32 v194, v160, v164
	v_cvt_pk_fp8_f32 v194, v168, v172 op_sel:[0,0,1]
	v_cvt_pk_fp8_f32 v195, v176, v180
	v_cvt_pk_fp8_f32 v195, v184, v188 op_sel:[0,0,1]
	global_store_dwordx4 v209, v[192:195], s[24:25] sc1
	v_cvt_pk_fp8_f32 v196, v129, v133
	v_cvt_pk_fp8_f32 v196, v137, v141 op_sel:[0,0,1]
	v_cvt_pk_fp8_f32 v197, v145, v149
	v_cvt_pk_fp8_f32 v197, v153, v157 op_sel:[0,0,1]
	v_cvt_pk_fp8_f32 v198, v161, v165
	v_cvt_pk_fp8_f32 v198, v169, v173 op_sel:[0,0,1]
	v_cvt_pk_fp8_f32 v199, v177, v181
	v_cvt_pk_fp8_f32 v199, v185, v189 op_sel:[0,0,1]
	global_store_dwordx4 v209, v[196:199], s[24:25] offset:2048 sc1
	v_cvt_pk_fp8_f32 v200, v130, v134
	v_cvt_pk_fp8_f32 v200, v138, v142 op_sel:[0,0,1]
	v_cvt_pk_fp8_f32 v201, v146, v150
	v_cvt_pk_fp8_f32 v201, v154, v158 op_sel:[0,0,1]
	v_cvt_pk_fp8_f32 v202, v162, v166
	v_cvt_pk_fp8_f32 v202, v170, v174 op_sel:[0,0,1]
	v_cvt_pk_fp8_f32 v203, v178, v182
	v_cvt_pk_fp8_f32 v203, v186, v190 op_sel:[0,0,1]
	global_store_dwordx4 v209, v[200:203], s[26:27] sc1
	v_cvt_pk_fp8_f32 v204, v131, v135
	v_cvt_pk_fp8_f32 v204, v139, v143 op_sel:[0,0,1]
	v_cvt_pk_fp8_f32 v205, v147, v151
	v_cvt_pk_fp8_f32 v205, v155, v159 op_sel:[0,0,1]
	v_cvt_pk_fp8_f32 v206, v163, v167
	v_cvt_pk_fp8_f32 v206, v171, v175 op_sel:[0,0,1]
	v_cvt_pk_fp8_f32 v207, v179, v183
	v_cvt_pk_fp8_f32 v207, v187, v191 op_sel:[0,0,1]
	global_store_dwordx4 v209, v[204:207], s[26:27] offset:2048 sc1
	s_add_i32 s1, s20, 260
	s_lshr_b32 s2, s1, 10
	s_and_b32 s4, s1, 0x3ff
	s_lshr_b32 s5, s4, 6
	s_and_b32 s4, s4, 63
	s_lshl_b32 s12, s2, 24
	s_lshl_b32 s13, s5, 20
	s_add_i32 s12, s12, s13
	s_lshl_b32 s13, s4, 7
	s_add_i32 s12, s12, s13
	s_add_u32 s14, s70, s12
	s_addc_u32 s15, s71, 0
	global_load_dwordx4 v[128:131], v208, s[14:15] sc1 nt
	s_add_u32 s18, s14, 0x2000
	s_addc_u32 s19, s15, 0
	global_load_dwordx4 v[132:135], v208, s[18:19] sc1 nt
	s_add_u32 s18, s14, 0x4000
	s_addc_u32 s19, s15, 0
	global_load_dwordx4 v[136:139], v208, s[18:19] sc1 nt
	s_add_u32 s18, s14, 0x6000
	s_addc_u32 s19, s15, 0
	global_load_dwordx4 v[140:143], v208, s[18:19] sc1 nt
	s_add_u32 s18, s14, 0x8000
	s_addc_u32 s19, s15, 0
	global_load_dwordx4 v[144:147], v208, s[18:19] sc1 nt
	s_add_u32 s18, s14, 0xa000
	s_addc_u32 s19, s15, 0
	global_load_dwordx4 v[148:151], v208, s[18:19] sc1 nt
	s_add_u32 s18, s14, 0xc000
	s_addc_u32 s19, s15, 0
	global_load_dwordx4 v[152:155], v208, s[18:19] sc1 nt
	s_add_u32 s18, s14, 0xe000
	s_addc_u32 s19, s15, 0
	global_load_dwordx4 v[156:159], v208, s[18:19] sc1 nt
	s_add_u32 s18, s14, 0x10000
	s_addc_u32 s19, s15, 0
	global_load_dwordx4 v[160:163], v208, s[18:19] sc1 nt
	s_add_u32 s18, s14, 0x12000
	s_addc_u32 s19, s15, 0
	global_load_dwordx4 v[164:167], v208, s[18:19] sc1 nt
	s_add_u32 s18, s14, 0x14000
	s_addc_u32 s19, s15, 0
	global_load_dwordx4 v[168:171], v208, s[18:19] sc1 nt
	s_add_u32 s18, s14, 0x16000
	s_addc_u32 s19, s15, 0
	global_load_dwordx4 v[172:175], v208, s[18:19] sc1 nt
	s_add_u32 s18, s14, 0x18000
	s_addc_u32 s19, s15, 0
	global_load_dwordx4 v[176:179], v208, s[18:19] sc1 nt
	s_add_u32 s18, s14, 0x1a000
	s_addc_u32 s19, s15, 0
	global_load_dwordx4 v[180:183], v208, s[18:19] sc1 nt
	s_add_u32 s18, s14, 0x1c000
	s_addc_u32 s19, s15, 0
	global_load_dwordx4 v[184:187], v208, s[18:19] sc1 nt
	s_add_u32 s18, s14, 0x1e000
	s_addc_u32 s19, s15, 0
	global_load_dwordx4 v[188:191], v208, s[18:19] sc1 nt
	s_waitcnt vmcnt(40)
	s_add_i32 s1, s20, 258
	s_lshr_b32 s2, s1, 10
	s_and_b32 s4, s1, 0x3ff
	s_lshr_b32 s5, s4, 6
	s_and_b32 s4, s4, 63
	s_lshl_b32 s12, s2, 22
	s_lshl_b32 s13, s4, 16
	s_add_i32 s12, s12, s13
	s_lshl_b32 s13, s5, 7
	s_add_i32 s12, s12, s13
	s_add_u32 s24, s90, s12
	s_addc_u32 s25, s91, 0
	s_add_u32 s24, s24, 0x3b100000
	s_addc_u32 s25, s25, 0
	s_add_u32 s26, s24, 0x1000
	s_addc_u32 s27, s25, 0
	v_pk_mul_f32 v[0:1], v[0:1], s[16:17] op_sel_hi:[1,0]
	v_pk_mul_f32 v[2:3], v[2:3], s[16:17] op_sel_hi:[1,0]
	v_pk_mul_f32 v[4:5], v[4:5], s[16:17] op_sel_hi:[1,0]
	v_pk_mul_f32 v[6:7], v[6:7], s[16:17] op_sel_hi:[1,0]
	v_pk_mul_f32 v[8:9], v[8:9], s[16:17] op_sel_hi:[1,0]
	v_pk_mul_f32 v[10:11], v[10:11], s[16:17] op_sel_hi:[1,0]
	v_pk_mul_f32 v[12:13], v[12:13], s[16:17] op_sel_hi:[1,0]
	v_pk_mul_f32 v[14:15], v[14:15], s[16:17] op_sel_hi:[1,0]
	v_pk_mul_f32 v[16:17], v[16:17], s[16:17] op_sel_hi:[1,0]
	v_pk_mul_f32 v[18:19], v[18:19], s[16:17] op_sel_hi:[1,0]
	v_pk_mul_f32 v[20:21], v[20:21], s[16:17] op_sel_hi:[1,0]
	v_pk_mul_f32 v[22:23], v[22:23], s[16:17] op_sel_hi:[1,0]
	v_pk_mul_f32 v[24:25], v[24:25], s[16:17] op_sel_hi:[1,0]
	v_pk_mul_f32 v[26:27], v[26:27], s[16:17] op_sel_hi:[1,0]
	v_pk_mul_f32 v[28:29], v[28:29], s[16:17] op_sel_hi:[1,0]
	v_pk_mul_f32 v[30:31], v[30:31], s[16:17] op_sel_hi:[1,0]
	v_pk_mul_f32 v[32:33], v[32:33], s[16:17] op_sel_hi:[1,0]
	v_pk_mul_f32 v[34:35], v[34:35], s[16:17] op_sel_hi:[1,0]
	v_pk_mul_f32 v[36:37], v[36:37], s[16:17] op_sel_hi:[1,0]
	v_pk_mul_f32 v[38:39], v[38:39], s[16:17] op_sel_hi:[1,0]
	v_pk_mul_f32 v[40:41], v[40:41], s[16:17] op_sel_hi:[1,0]
	v_pk_mul_f32 v[42:43], v[42:43], s[16:17] op_sel_hi:[1,0]
	v_pk_mul_f32 v[44:45], v[44:45], s[16:17] op_sel_hi:[1,0]
	v_pk_mul_f32 v[46:47], v[46:47], s[16:17] op_sel_hi:[1,0]
	v_pk_mul_f32 v[48:49], v[48:49], s[16:17] op_sel_hi:[1,0]
	v_pk_mul_f32 v[50:51], v[50:51], s[16:17] op_sel_hi:[1,0]
	v_pk_mul_f32 v[52:53], v[52:53], s[16:17] op_sel_hi:[1,0]
	v_pk_mul_f32 v[54:55], v[54:55], s[16:17] op_sel_hi:[1,0]
	v_pk_mul_f32 v[56:57], v[56:57], s[16:17] op_sel_hi:[1,0]
	v_pk_mul_f32 v[58:59], v[58:59], s[16:17] op_sel_hi:[1,0]
	v_pk_mul_f32 v[60:61], v[60:61], s[16:17] op_sel_hi:[1,0]
	v_pk_mul_f32 v[62:63], v[62:63], s[16:17] op_sel_hi:[1,0]
	v_cvt_pk_fp8_f32 v192, v0, v4
	v_cvt_pk_fp8_f32 v192, v8, v12 op_sel:[0,0,1]
	v_cvt_pk_fp8_f32 v193, v16, v20
	v_cvt_pk_fp8_f32 v193, v24, v28 op_sel:[0,0,1]
	v_cvt_pk_fp8_f32 v194, v32, v36
	v_cvt_pk_fp8_f32 v194, v40, v44 op_sel:[0,0,1]
	v_cvt_pk_fp8_f32 v195, v48, v52
	v_cvt_pk_fp8_f32 v195, v56, v60 op_sel:[0,0,1]
	global_store_dwordx4 v209, v[192:195], s[24:25] sc1
	v_cvt_pk_fp8_f32 v196, v1, v5
	v_cvt_pk_fp8_f32 v196, v9, v13 op_sel:[0,0,1]
	v_cvt_pk_fp8_f32 v197, v17, v21
	v_cvt_pk_fp8_f32 v197, v25, v29 op_sel:[0,0,1]
	v_cvt_pk_fp8_f32 v198, v33, v37
	v_cvt_pk_fp8_f32 v198, v41, v45 op_sel:[0,0,1]
	v_cvt_pk_fp8_f32 v199, v49, v53
	v_cvt_pk_fp8_f32 v199, v57, v61 op_sel:[0,0,1]
	global_store_dwordx4 v209, v[196:199], s[24:25] offset:2048 sc1
	v_cvt_pk_fp8_f32 v200, v2, v6
	v_cvt_pk_fp8_f32 v200, v10, v14 op_sel:[0,0,1]
	v_cvt_pk_fp8_f32 v201, v18, v22
	v_cvt_pk_fp8_f32 v201, v26, v30 op_sel:[0,0,1]
	v_cvt_pk_fp8_f32 v202, v34, v38
	v_cvt_pk_fp8_f32 v202, v42, v46 op_sel:[0,0,1]
	v_cvt_pk_fp8_f32 v203, v50, v54
	v_cvt_pk_fp8_f32 v203, v58, v62 op_sel:[0,0,1]
	global_store_dwordx4 v209, v[200:203], s[26:27] sc1
	v_cvt_pk_fp8_f32 v204, v3, v7
	v_cvt_pk_fp8_f32 v204, v11, v15 op_sel:[0,0,1]
	v_cvt_pk_fp8_f32 v205, v19, v23
	v_cvt_pk_fp8_f32 v205, v27, v31 op_sel:[0,0,1]
	v_cvt_pk_fp8_f32 v206, v35, v39
	v_cvt_pk_fp8_f32 v206, v43, v47 op_sel:[0,0,1]
	v_cvt_pk_fp8_f32 v207, v51, v55
	v_cvt_pk_fp8_f32 v207, v59, v63 op_sel:[0,0,1]
	global_store_dwordx4 v209, v[204:207], s[26:27] offset:2048 sc1
	s_add_i32 s1, s20, 6
	s_lshr_b32 s2, s1, 10
	s_and_b32 s4, s1, 0x3ff
	s_lshr_b32 s5, s4, 6
	s_and_b32 s4, s4, 63
	s_lshl_b32 s12, s2, 24
	s_lshl_b32 s13, s5, 20
	s_add_i32 s12, s12, s13
	s_lshl_b32 s13, s4, 7
	s_add_i32 s12, s12, s13
	s_add_u32 s14, s70, s12
	s_addc_u32 s15, s71, 0
	global_load_dwordx4 v[0:3], v208, s[14:15] sc1 nt
	s_add_u32 s18, s14, 0x2000
	s_addc_u32 s19, s15, 0
	global_load_dwordx4 v[4:7], v208, s[18:19] sc1 nt
	s_add_u32 s18, s14, 0x4000
	s_addc_u32 s19, s15, 0
	global_load_dwordx4 v[8:11], v208, s[18:19] sc1 nt
	s_add_u32 s18, s14, 0x6000
	s_addc_u32 s19, s15, 0
	global_load_dwordx4 v[12:15], v208, s[18:19] sc1 nt
	s_add_u32 s18, s14, 0x8000
	s_addc_u32 s19, s15, 0
	global_load_dwordx4 v[16:19], v208, s[18:19] sc1 nt
	s_add_u32 s18, s14, 0xa000
	s_addc_u32 s19, s15, 0
	global_load_dwordx4 v[20:23], v208, s[18:19] sc1 nt
	s_add_u32 s18, s14, 0xc000
	s_addc_u32 s19, s15, 0
	global_load_dwordx4 v[24:27], v208, s[18:19] sc1 nt
	s_add_u32 s18, s14, 0xe000
	s_addc_u32 s19, s15, 0
	global_load_dwordx4 v[28:31], v208, s[18:19] sc1 nt
	s_add_u32 s18, s14, 0x10000
	s_addc_u32 s19, s15, 0
	global_load_dwordx4 v[32:35], v208, s[18:19] sc1 nt
	s_add_u32 s18, s14, 0x12000
	s_addc_u32 s19, s15, 0
	global_load_dwordx4 v[36:39], v208, s[18:19] sc1 nt
	s_add_u32 s18, s14, 0x14000
	s_addc_u32 s19, s15, 0
	global_load_dwordx4 v[40:43], v208, s[18:19] sc1 nt
	s_add_u32 s18, s14, 0x16000
	s_addc_u32 s19, s15, 0
	global_load_dwordx4 v[44:47], v208, s[18:19] sc1 nt
	s_add_u32 s18, s14, 0x18000
	s_addc_u32 s19, s15, 0
	global_load_dwordx4 v[48:51], v208, s[18:19] sc1 nt
	s_add_u32 s18, s14, 0x1a000
	s_addc_u32 s19, s15, 0
	global_load_dwordx4 v[52:55], v208, s[18:19] sc1 nt
	s_add_u32 s18, s14, 0x1c000
	s_addc_u32 s19, s15, 0
	global_load_dwordx4 v[56:59], v208, s[18:19] sc1 nt
	s_add_u32 s18, s14, 0x1e000
	s_addc_u32 s19, s15, 0
	global_load_dwordx4 v[60:63], v208, s[18:19] sc1 nt
	s_waitcnt vmcnt(40)
	s_add_i32 s1, s20, 4
	s_lshr_b32 s2, s1, 10
	s_and_b32 s4, s1, 0x3ff
	s_lshr_b32 s5, s4, 6
	s_and_b32 s4, s4, 63
	s_lshl_b32 s12, s2, 22
	s_lshl_b32 s13, s4, 16
	s_add_i32 s12, s12, s13
	s_lshl_b32 s13, s5, 7
	s_add_i32 s12, s12, s13
	s_add_u32 s24, s90, s12
	s_addc_u32 s25, s91, 0
	s_add_u32 s24, s24, 0x3b100000
	s_addc_u32 s25, s25, 0
	s_add_u32 s26, s24, 0x1000
	s_addc_u32 s27, s25, 0
	v_pk_mul_f32 v[64:65], v[64:65], s[16:17] op_sel_hi:[1,0]
	v_pk_mul_f32 v[66:67], v[66:67], s[16:17] op_sel_hi:[1,0]
	v_pk_mul_f32 v[68:69], v[68:69], s[16:17] op_sel_hi:[1,0]
	v_pk_mul_f32 v[70:71], v[70:71], s[16:17] op_sel_hi:[1,0]
	v_pk_mul_f32 v[72:73], v[72:73], s[16:17] op_sel_hi:[1,0]
	v_pk_mul_f32 v[74:75], v[74:75], s[16:17] op_sel_hi:[1,0]
	v_pk_mul_f32 v[76:77], v[76:77], s[16:17] op_sel_hi:[1,0]
	v_pk_mul_f32 v[78:79], v[78:79], s[16:17] op_sel_hi:[1,0]
	v_pk_mul_f32 v[80:81], v[80:81], s[16:17] op_sel_hi:[1,0]
	v_pk_mul_f32 v[82:83], v[82:83], s[16:17] op_sel_hi:[1,0]
	v_pk_mul_f32 v[84:85], v[84:85], s[16:17] op_sel_hi:[1,0]
	v_pk_mul_f32 v[86:87], v[86:87], s[16:17] op_sel_hi:[1,0]
	v_pk_mul_f32 v[88:89], v[88:89], s[16:17] op_sel_hi:[1,0]
	v_pk_mul_f32 v[90:91], v[90:91], s[16:17] op_sel_hi:[1,0]
	v_pk_mul_f32 v[92:93], v[92:93], s[16:17] op_sel_hi:[1,0]
	v_pk_mul_f32 v[94:95], v[94:95], s[16:17] op_sel_hi:[1,0]
	v_pk_mul_f32 v[96:97], v[96:97], s[16:17] op_sel_hi:[1,0]
	v_pk_mul_f32 v[98:99], v[98:99], s[16:17] op_sel_hi:[1,0]
	v_pk_mul_f32 v[100:101], v[100:101], s[16:17] op_sel_hi:[1,0]
	v_pk_mul_f32 v[102:103], v[102:103], s[16:17] op_sel_hi:[1,0]
	v_pk_mul_f32 v[104:105], v[104:105], s[16:17] op_sel_hi:[1,0]
	v_pk_mul_f32 v[106:107], v[106:107], s[16:17] op_sel_hi:[1,0]
	v_pk_mul_f32 v[108:109], v[108:109], s[16:17] op_sel_hi:[1,0]
	v_pk_mul_f32 v[110:111], v[110:111], s[16:17] op_sel_hi:[1,0]
	v_pk_mul_f32 v[112:113], v[112:113], s[16:17] op_sel_hi:[1,0]
	v_pk_mul_f32 v[114:115], v[114:115], s[16:17] op_sel_hi:[1,0]
	v_pk_mul_f32 v[116:117], v[116:117], s[16:17] op_sel_hi:[1,0]
	v_pk_mul_f32 v[118:119], v[118:119], s[16:17] op_sel_hi:[1,0]
	v_pk_mul_f32 v[120:121], v[120:121], s[16:17] op_sel_hi:[1,0]
	v_pk_mul_f32 v[122:123], v[122:123], s[16:17] op_sel_hi:[1,0]
	v_pk_mul_f32 v[124:125], v[124:125], s[16:17] op_sel_hi:[1,0]
	v_pk_mul_f32 v[126:127], v[126:127], s[16:17] op_sel_hi:[1,0]
	v_cvt_pk_fp8_f32 v192, v64, v68
	v_cvt_pk_fp8_f32 v192, v72, v76 op_sel:[0,0,1]
	v_cvt_pk_fp8_f32 v193, v80, v84
	v_cvt_pk_fp8_f32 v193, v88, v92 op_sel:[0,0,1]
	v_cvt_pk_fp8_f32 v194, v96, v100
	v_cvt_pk_fp8_f32 v194, v104, v108 op_sel:[0,0,1]
	v_cvt_pk_fp8_f32 v195, v112, v116
	v_cvt_pk_fp8_f32 v195, v120, v124 op_sel:[0,0,1]
	global_store_dwordx4 v209, v[192:195], s[24:25] sc1
	v_cvt_pk_fp8_f32 v196, v65, v69
	v_cvt_pk_fp8_f32 v196, v73, v77 op_sel:[0,0,1]
	v_cvt_pk_fp8_f32 v197, v81, v85
	v_cvt_pk_fp8_f32 v197, v89, v93 op_sel:[0,0,1]
	v_cvt_pk_fp8_f32 v198, v97, v101
	v_cvt_pk_fp8_f32 v198, v105, v109 op_sel:[0,0,1]
	v_cvt_pk_fp8_f32 v199, v113, v117
	v_cvt_pk_fp8_f32 v199, v121, v125 op_sel:[0,0,1]
	global_store_dwordx4 v209, v[196:199], s[24:25] offset:2048 sc1
	v_cvt_pk_fp8_f32 v200, v66, v70
	v_cvt_pk_fp8_f32 v200, v74, v78 op_sel:[0,0,1]
	v_cvt_pk_fp8_f32 v201, v82, v86
	v_cvt_pk_fp8_f32 v201, v90, v94 op_sel:[0,0,1]
	v_cvt_pk_fp8_f32 v202, v98, v102
	v_cvt_pk_fp8_f32 v202, v106, v110 op_sel:[0,0,1]
	v_cvt_pk_fp8_f32 v203, v114, v118
	v_cvt_pk_fp8_f32 v203, v122, v126 op_sel:[0,0,1]
	global_store_dwordx4 v209, v[200:203], s[26:27] sc1
	v_cvt_pk_fp8_f32 v204, v67, v71
	v_cvt_pk_fp8_f32 v204, v75, v79 op_sel:[0,0,1]
	v_cvt_pk_fp8_f32 v205, v83, v87
	v_cvt_pk_fp8_f32 v205, v91, v95 op_sel:[0,0,1]
	v_cvt_pk_fp8_f32 v206, v99, v103
	v_cvt_pk_fp8_f32 v206, v107, v111 op_sel:[0,0,1]
	v_cvt_pk_fp8_f32 v207, v115, v119
	v_cvt_pk_fp8_f32 v207, v123, v127 op_sel:[0,0,1]
	global_store_dwordx4 v209, v[204:207], s[26:27] offset:2048 sc1
	s_add_i32 s1, s20, 262
	s_lshr_b32 s2, s1, 10
	s_and_b32 s4, s1, 0x3ff
	s_lshr_b32 s5, s4, 6
	s_and_b32 s4, s4, 63
	s_lshl_b32 s12, s2, 24
	s_lshl_b32 s13, s5, 20
	s_add_i32 s12, s12, s13
	s_lshl_b32 s13, s4, 7
	s_add_i32 s12, s12, s13
	s_add_u32 s14, s70, s12
	s_addc_u32 s15, s71, 0
	global_load_dwordx4 v[64:67], v208, s[14:15] sc1 nt
	s_add_u32 s18, s14, 0x2000
	s_addc_u32 s19, s15, 0
	global_load_dwordx4 v[68:71], v208, s[18:19] sc1 nt
	s_add_u32 s18, s14, 0x4000
	s_addc_u32 s19, s15, 0
	global_load_dwordx4 v[72:75], v208, s[18:19] sc1 nt
	s_add_u32 s18, s14, 0x6000
	s_addc_u32 s19, s15, 0
	global_load_dwordx4 v[76:79], v208, s[18:19] sc1 nt
	s_add_u32 s18, s14, 0x8000
	s_addc_u32 s19, s15, 0
	global_load_dwordx4 v[80:83], v208, s[18:19] sc1 nt
	s_add_u32 s18, s14, 0xa000
	s_addc_u32 s19, s15, 0
	global_load_dwordx4 v[84:87], v208, s[18:19] sc1 nt
	s_add_u32 s18, s14, 0xc000
	s_addc_u32 s19, s15, 0
	global_load_dwordx4 v[88:91], v208, s[18:19] sc1 nt
	s_add_u32 s18, s14, 0xe000
	s_addc_u32 s19, s15, 0
	global_load_dwordx4 v[92:95], v208, s[18:19] sc1 nt
	s_add_u32 s18, s14, 0x10000
	s_addc_u32 s19, s15, 0
	global_load_dwordx4 v[96:99], v208, s[18:19] sc1 nt
	s_add_u32 s18, s14, 0x12000
	s_addc_u32 s19, s15, 0
	global_load_dwordx4 v[100:103], v208, s[18:19] sc1 nt
	s_add_u32 s18, s14, 0x14000
	s_addc_u32 s19, s15, 0
	global_load_dwordx4 v[104:107], v208, s[18:19] sc1 nt
	s_add_u32 s18, s14, 0x16000
	s_addc_u32 s19, s15, 0
	global_load_dwordx4 v[108:111], v208, s[18:19] sc1 nt
	s_add_u32 s18, s14, 0x18000
	s_addc_u32 s19, s15, 0
	global_load_dwordx4 v[112:115], v208, s[18:19] sc1 nt
	s_add_u32 s18, s14, 0x1a000
	s_addc_u32 s19, s15, 0
	global_load_dwordx4 v[116:119], v208, s[18:19] sc1 nt
	s_add_u32 s18, s14, 0x1c000
	s_addc_u32 s19, s15, 0
	global_load_dwordx4 v[120:123], v208, s[18:19] sc1 nt
	s_add_u32 s18, s14, 0x1e000
	s_addc_u32 s19, s15, 0
	global_load_dwordx4 v[124:127], v208, s[18:19] sc1 nt
	s_waitcnt vmcnt(40)
	s_add_i32 s1, s20, 260
	s_lshr_b32 s2, s1, 10
	s_and_b32 s4, s1, 0x3ff
	s_lshr_b32 s5, s4, 6
	s_and_b32 s4, s4, 63
	s_lshl_b32 s12, s2, 22
	s_lshl_b32 s13, s4, 16
	s_add_i32 s12, s12, s13
	s_lshl_b32 s13, s5, 7
	s_add_i32 s12, s12, s13
	s_add_u32 s24, s90, s12
	s_addc_u32 s25, s91, 0
	s_add_u32 s24, s24, 0x3b100000
	s_addc_u32 s25, s25, 0
	s_add_u32 s26, s24, 0x1000
	s_addc_u32 s27, s25, 0
	v_pk_mul_f32 v[128:129], v[128:129], s[16:17] op_sel_hi:[1,0]
	v_pk_mul_f32 v[130:131], v[130:131], s[16:17] op_sel_hi:[1,0]
	v_pk_mul_f32 v[132:133], v[132:133], s[16:17] op_sel_hi:[1,0]
	v_pk_mul_f32 v[134:135], v[134:135], s[16:17] op_sel_hi:[1,0]
	v_pk_mul_f32 v[136:137], v[136:137], s[16:17] op_sel_hi:[1,0]
	v_pk_mul_f32 v[138:139], v[138:139], s[16:17] op_sel_hi:[1,0]
	v_pk_mul_f32 v[140:141], v[140:141], s[16:17] op_sel_hi:[1,0]
	v_pk_mul_f32 v[142:143], v[142:143], s[16:17] op_sel_hi:[1,0]
	v_pk_mul_f32 v[144:145], v[144:145], s[16:17] op_sel_hi:[1,0]
	v_pk_mul_f32 v[146:147], v[146:147], s[16:17] op_sel_hi:[1,0]
	v_pk_mul_f32 v[148:149], v[148:149], s[16:17] op_sel_hi:[1,0]
	v_pk_mul_f32 v[150:151], v[150:151], s[16:17] op_sel_hi:[1,0]
	v_pk_mul_f32 v[152:153], v[152:153], s[16:17] op_sel_hi:[1,0]
	v_pk_mul_f32 v[154:155], v[154:155], s[16:17] op_sel_hi:[1,0]
	v_pk_mul_f32 v[156:157], v[156:157], s[16:17] op_sel_hi:[1,0]
	v_pk_mul_f32 v[158:159], v[158:159], s[16:17] op_sel_hi:[1,0]
	v_pk_mul_f32 v[160:161], v[160:161], s[16:17] op_sel_hi:[1,0]
	v_pk_mul_f32 v[162:163], v[162:163], s[16:17] op_sel_hi:[1,0]
	v_pk_mul_f32 v[164:165], v[164:165], s[16:17] op_sel_hi:[1,0]
	v_pk_mul_f32 v[166:167], v[166:167], s[16:17] op_sel_hi:[1,0]
	v_pk_mul_f32 v[168:169], v[168:169], s[16:17] op_sel_hi:[1,0]
	v_pk_mul_f32 v[170:171], v[170:171], s[16:17] op_sel_hi:[1,0]
	v_pk_mul_f32 v[172:173], v[172:173], s[16:17] op_sel_hi:[1,0]
	v_pk_mul_f32 v[174:175], v[174:175], s[16:17] op_sel_hi:[1,0]
	v_pk_mul_f32 v[176:177], v[176:177], s[16:17] op_sel_hi:[1,0]
	v_pk_mul_f32 v[178:179], v[178:179], s[16:17] op_sel_hi:[1,0]
	v_pk_mul_f32 v[180:181], v[180:181], s[16:17] op_sel_hi:[1,0]
	v_pk_mul_f32 v[182:183], v[182:183], s[16:17] op_sel_hi:[1,0]
	v_pk_mul_f32 v[184:185], v[184:185], s[16:17] op_sel_hi:[1,0]
	v_pk_mul_f32 v[186:187], v[186:187], s[16:17] op_sel_hi:[1,0]
	v_pk_mul_f32 v[188:189], v[188:189], s[16:17] op_sel_hi:[1,0]
	v_pk_mul_f32 v[190:191], v[190:191], s[16:17] op_sel_hi:[1,0]
	v_cvt_pk_fp8_f32 v192, v128, v132
	v_cvt_pk_fp8_f32 v192, v136, v140 op_sel:[0,0,1]
	v_cvt_pk_fp8_f32 v193, v144, v148
	v_cvt_pk_fp8_f32 v193, v152, v156 op_sel:[0,0,1]
	v_cvt_pk_fp8_f32 v194, v160, v164
	v_cvt_pk_fp8_f32 v194, v168, v172 op_sel:[0,0,1]
	v_cvt_pk_fp8_f32 v195, v176, v180
	v_cvt_pk_fp8_f32 v195, v184, v188 op_sel:[0,0,1]
	global_store_dwordx4 v209, v[192:195], s[24:25] sc1
	v_cvt_pk_fp8_f32 v196, v129, v133
	v_cvt_pk_fp8_f32 v196, v137, v141 op_sel:[0,0,1]
	v_cvt_pk_fp8_f32 v197, v145, v149
	v_cvt_pk_fp8_f32 v197, v153, v157 op_sel:[0,0,1]
	v_cvt_pk_fp8_f32 v198, v161, v165
	v_cvt_pk_fp8_f32 v198, v169, v173 op_sel:[0,0,1]
	v_cvt_pk_fp8_f32 v199, v177, v181
	v_cvt_pk_fp8_f32 v199, v185, v189 op_sel:[0,0,1]
	global_store_dwordx4 v209, v[196:199], s[24:25] offset:2048 sc1
	v_cvt_pk_fp8_f32 v200, v130, v134
	v_cvt_pk_fp8_f32 v200, v138, v142 op_sel:[0,0,1]
	v_cvt_pk_fp8_f32 v201, v146, v150
	v_cvt_pk_fp8_f32 v201, v154, v158 op_sel:[0,0,1]
	v_cvt_pk_fp8_f32 v202, v162, v166
	v_cvt_pk_fp8_f32 v202, v170, v174 op_sel:[0,0,1]
	v_cvt_pk_fp8_f32 v203, v178, v182
	v_cvt_pk_fp8_f32 v203, v186, v190 op_sel:[0,0,1]
	global_store_dwordx4 v209, v[200:203], s[26:27] sc1
	v_cvt_pk_fp8_f32 v204, v131, v135
	v_cvt_pk_fp8_f32 v204, v139, v143 op_sel:[0,0,1]
	v_cvt_pk_fp8_f32 v205, v147, v151
	v_cvt_pk_fp8_f32 v205, v155, v159 op_sel:[0,0,1]
	v_cvt_pk_fp8_f32 v206, v163, v167
	v_cvt_pk_fp8_f32 v206, v171, v175 op_sel:[0,0,1]
	v_cvt_pk_fp8_f32 v207, v179, v183
	v_cvt_pk_fp8_f32 v207, v187, v191 op_sel:[0,0,1]
	global_store_dwordx4 v209, v[204:207], s[26:27] offset:2048 sc1
	s_add_i32 s1, s20, 8
	s_lshr_b32 s2, s1, 10
	s_and_b32 s4, s1, 0x3ff
	s_lshr_b32 s5, s4, 6
	s_and_b32 s4, s4, 63
	s_lshl_b32 s12, s2, 24
	s_lshl_b32 s13, s5, 20
	s_add_i32 s12, s12, s13
	s_lshl_b32 s13, s4, 7
	s_add_i32 s12, s12, s13
	s_add_u32 s14, s70, s12
	s_addc_u32 s15, s71, 0
	global_load_dwordx4 v[128:131], v208, s[14:15] sc1 nt
	s_add_u32 s18, s14, 0x2000
	s_addc_u32 s19, s15, 0
	global_load_dwordx4 v[132:135], v208, s[18:19] sc1 nt
	s_add_u32 s18, s14, 0x4000
	s_addc_u32 s19, s15, 0
	global_load_dwordx4 v[136:139], v208, s[18:19] sc1 nt
	s_add_u32 s18, s14, 0x6000
	s_addc_u32 s19, s15, 0
	global_load_dwordx4 v[140:143], v208, s[18:19] sc1 nt
	s_add_u32 s18, s14, 0x8000
	s_addc_u32 s19, s15, 0
	global_load_dwordx4 v[144:147], v208, s[18:19] sc1 nt
	s_add_u32 s18, s14, 0xa000
	s_addc_u32 s19, s15, 0
	global_load_dwordx4 v[148:151], v208, s[18:19] sc1 nt
	s_add_u32 s18, s14, 0xc000
	s_addc_u32 s19, s15, 0
	global_load_dwordx4 v[152:155], v208, s[18:19] sc1 nt
	s_add_u32 s18, s14, 0xe000
	s_addc_u32 s19, s15, 0
	global_load_dwordx4 v[156:159], v208, s[18:19] sc1 nt
	s_add_u32 s18, s14, 0x10000
	s_addc_u32 s19, s15, 0
	global_load_dwordx4 v[160:163], v208, s[18:19] sc1 nt
	s_add_u32 s18, s14, 0x12000
	s_addc_u32 s19, s15, 0
	global_load_dwordx4 v[164:167], v208, s[18:19] sc1 nt
	s_add_u32 s18, s14, 0x14000
	s_addc_u32 s19, s15, 0
	global_load_dwordx4 v[168:171], v208, s[18:19] sc1 nt
	s_add_u32 s18, s14, 0x16000
	s_addc_u32 s19, s15, 0
	global_load_dwordx4 v[172:175], v208, s[18:19] sc1 nt
	s_add_u32 s18, s14, 0x18000
	s_addc_u32 s19, s15, 0
	global_load_dwordx4 v[176:179], v208, s[18:19] sc1 nt
	s_add_u32 s18, s14, 0x1a000
	s_addc_u32 s19, s15, 0
	global_load_dwordx4 v[180:183], v208, s[18:19] sc1 nt
	s_add_u32 s18, s14, 0x1c000
	s_addc_u32 s19, s15, 0
	global_load_dwordx4 v[184:187], v208, s[18:19] sc1 nt
	s_add_u32 s18, s14, 0x1e000
	s_addc_u32 s19, s15, 0
	global_load_dwordx4 v[188:191], v208, s[18:19] sc1 nt
	s_waitcnt vmcnt(40)
	s_add_i32 s1, s20, 6
	s_lshr_b32 s2, s1, 10
	s_and_b32 s4, s1, 0x3ff
	s_lshr_b32 s5, s4, 6
	s_and_b32 s4, s4, 63
	s_lshl_b32 s12, s2, 22
	s_lshl_b32 s13, s4, 16
	s_add_i32 s12, s12, s13
	s_lshl_b32 s13, s5, 7
	s_add_i32 s12, s12, s13
	s_add_u32 s24, s90, s12
	s_addc_u32 s25, s91, 0
	s_add_u32 s24, s24, 0x3b100000
	s_addc_u32 s25, s25, 0
	s_add_u32 s26, s24, 0x1000
	s_addc_u32 s27, s25, 0
	v_pk_mul_f32 v[0:1], v[0:1], s[16:17] op_sel_hi:[1,0]
	v_pk_mul_f32 v[2:3], v[2:3], s[16:17] op_sel_hi:[1,0]
	v_pk_mul_f32 v[4:5], v[4:5], s[16:17] op_sel_hi:[1,0]
	v_pk_mul_f32 v[6:7], v[6:7], s[16:17] op_sel_hi:[1,0]
	v_pk_mul_f32 v[8:9], v[8:9], s[16:17] op_sel_hi:[1,0]
	v_pk_mul_f32 v[10:11], v[10:11], s[16:17] op_sel_hi:[1,0]
	v_pk_mul_f32 v[12:13], v[12:13], s[16:17] op_sel_hi:[1,0]
	v_pk_mul_f32 v[14:15], v[14:15], s[16:17] op_sel_hi:[1,0]
	v_pk_mul_f32 v[16:17], v[16:17], s[16:17] op_sel_hi:[1,0]
	v_pk_mul_f32 v[18:19], v[18:19], s[16:17] op_sel_hi:[1,0]
	v_pk_mul_f32 v[20:21], v[20:21], s[16:17] op_sel_hi:[1,0]
	v_pk_mul_f32 v[22:23], v[22:23], s[16:17] op_sel_hi:[1,0]
	v_pk_mul_f32 v[24:25], v[24:25], s[16:17] op_sel_hi:[1,0]
	v_pk_mul_f32 v[26:27], v[26:27], s[16:17] op_sel_hi:[1,0]
	v_pk_mul_f32 v[28:29], v[28:29], s[16:17] op_sel_hi:[1,0]
	v_pk_mul_f32 v[30:31], v[30:31], s[16:17] op_sel_hi:[1,0]
	v_pk_mul_f32 v[32:33], v[32:33], s[16:17] op_sel_hi:[1,0]
	v_pk_mul_f32 v[34:35], v[34:35], s[16:17] op_sel_hi:[1,0]
	v_pk_mul_f32 v[36:37], v[36:37], s[16:17] op_sel_hi:[1,0]
	v_pk_mul_f32 v[38:39], v[38:39], s[16:17] op_sel_hi:[1,0]
	v_pk_mul_f32 v[40:41], v[40:41], s[16:17] op_sel_hi:[1,0]
	v_pk_mul_f32 v[42:43], v[42:43], s[16:17] op_sel_hi:[1,0]
	v_pk_mul_f32 v[44:45], v[44:45], s[16:17] op_sel_hi:[1,0]
	v_pk_mul_f32 v[46:47], v[46:47], s[16:17] op_sel_hi:[1,0]
	v_pk_mul_f32 v[48:49], v[48:49], s[16:17] op_sel_hi:[1,0]
	v_pk_mul_f32 v[50:51], v[50:51], s[16:17] op_sel_hi:[1,0]
	v_pk_mul_f32 v[52:53], v[52:53], s[16:17] op_sel_hi:[1,0]
	v_pk_mul_f32 v[54:55], v[54:55], s[16:17] op_sel_hi:[1,0]
	v_pk_mul_f32 v[56:57], v[56:57], s[16:17] op_sel_hi:[1,0]
	v_pk_mul_f32 v[58:59], v[58:59], s[16:17] op_sel_hi:[1,0]
	v_pk_mul_f32 v[60:61], v[60:61], s[16:17] op_sel_hi:[1,0]
	v_pk_mul_f32 v[62:63], v[62:63], s[16:17] op_sel_hi:[1,0]
	v_cvt_pk_fp8_f32 v192, v0, v4
	v_cvt_pk_fp8_f32 v192, v8, v12 op_sel:[0,0,1]
	v_cvt_pk_fp8_f32 v193, v16, v20
	v_cvt_pk_fp8_f32 v193, v24, v28 op_sel:[0,0,1]
	v_cvt_pk_fp8_f32 v194, v32, v36
	v_cvt_pk_fp8_f32 v194, v40, v44 op_sel:[0,0,1]
	v_cvt_pk_fp8_f32 v195, v48, v52
	v_cvt_pk_fp8_f32 v195, v56, v60 op_sel:[0,0,1]
	global_store_dwordx4 v209, v[192:195], s[24:25] sc1
	v_cvt_pk_fp8_f32 v196, v1, v5
	v_cvt_pk_fp8_f32 v196, v9, v13 op_sel:[0,0,1]
	v_cvt_pk_fp8_f32 v197, v17, v21
	v_cvt_pk_fp8_f32 v197, v25, v29 op_sel:[0,0,1]
	v_cvt_pk_fp8_f32 v198, v33, v37
	v_cvt_pk_fp8_f32 v198, v41, v45 op_sel:[0,0,1]
	v_cvt_pk_fp8_f32 v199, v49, v53
	v_cvt_pk_fp8_f32 v199, v57, v61 op_sel:[0,0,1]
	global_store_dwordx4 v209, v[196:199], s[24:25] offset:2048 sc1
	v_cvt_pk_fp8_f32 v200, v2, v6
	v_cvt_pk_fp8_f32 v200, v10, v14 op_sel:[0,0,1]
	v_cvt_pk_fp8_f32 v201, v18, v22
	v_cvt_pk_fp8_f32 v201, v26, v30 op_sel:[0,0,1]
	v_cvt_pk_fp8_f32 v202, v34, v38
	v_cvt_pk_fp8_f32 v202, v42, v46 op_sel:[0,0,1]
	v_cvt_pk_fp8_f32 v203, v50, v54
	v_cvt_pk_fp8_f32 v203, v58, v62 op_sel:[0,0,1]
	global_store_dwordx4 v209, v[200:203], s[26:27] sc1
	v_cvt_pk_fp8_f32 v204, v3, v7
	v_cvt_pk_fp8_f32 v204, v11, v15 op_sel:[0,0,1]
	v_cvt_pk_fp8_f32 v205, v19, v23
	v_cvt_pk_fp8_f32 v205, v27, v31 op_sel:[0,0,1]
	v_cvt_pk_fp8_f32 v206, v35, v39
	v_cvt_pk_fp8_f32 v206, v43, v47 op_sel:[0,0,1]
	v_cvt_pk_fp8_f32 v207, v51, v55
	v_cvt_pk_fp8_f32 v207, v59, v63 op_sel:[0,0,1]
	global_store_dwordx4 v209, v[204:207], s[26:27] offset:2048 sc1
	s_add_i32 s1, s20, 264
	s_lshr_b32 s2, s1, 10
	s_and_b32 s4, s1, 0x3ff
	s_lshr_b32 s5, s4, 6
	s_and_b32 s4, s4, 63
	s_lshl_b32 s12, s2, 24
	s_lshl_b32 s13, s5, 20
	s_add_i32 s12, s12, s13
	s_lshl_b32 s13, s4, 7
	s_add_i32 s12, s12, s13
	s_add_u32 s14, s70, s12
	s_addc_u32 s15, s71, 0
	global_load_dwordx4 v[0:3], v208, s[14:15] sc1 nt
	s_add_u32 s18, s14, 0x2000
	s_addc_u32 s19, s15, 0
	global_load_dwordx4 v[4:7], v208, s[18:19] sc1 nt
	s_add_u32 s18, s14, 0x4000
	s_addc_u32 s19, s15, 0
	global_load_dwordx4 v[8:11], v208, s[18:19] sc1 nt
	s_add_u32 s18, s14, 0x6000
	s_addc_u32 s19, s15, 0
	global_load_dwordx4 v[12:15], v208, s[18:19] sc1 nt
	s_add_u32 s18, s14, 0x8000
	s_addc_u32 s19, s15, 0
	global_load_dwordx4 v[16:19], v208, s[18:19] sc1 nt
	s_add_u32 s18, s14, 0xa000
	s_addc_u32 s19, s15, 0
	global_load_dwordx4 v[20:23], v208, s[18:19] sc1 nt
	s_add_u32 s18, s14, 0xc000
	s_addc_u32 s19, s15, 0
	global_load_dwordx4 v[24:27], v208, s[18:19] sc1 nt
	s_add_u32 s18, s14, 0xe000
	s_addc_u32 s19, s15, 0
	global_load_dwordx4 v[28:31], v208, s[18:19] sc1 nt
	s_add_u32 s18, s14, 0x10000
	s_addc_u32 s19, s15, 0
	global_load_dwordx4 v[32:35], v208, s[18:19] sc1 nt
	s_add_u32 s18, s14, 0x12000
	s_addc_u32 s19, s15, 0
	global_load_dwordx4 v[36:39], v208, s[18:19] sc1 nt
	s_add_u32 s18, s14, 0x14000
	s_addc_u32 s19, s15, 0
	global_load_dwordx4 v[40:43], v208, s[18:19] sc1 nt
	s_add_u32 s18, s14, 0x16000
	s_addc_u32 s19, s15, 0
	global_load_dwordx4 v[44:47], v208, s[18:19] sc1 nt
	s_add_u32 s18, s14, 0x18000
	s_addc_u32 s19, s15, 0
	global_load_dwordx4 v[48:51], v208, s[18:19] sc1 nt
	s_add_u32 s18, s14, 0x1a000
	s_addc_u32 s19, s15, 0
	global_load_dwordx4 v[52:55], v208, s[18:19] sc1 nt
	s_add_u32 s18, s14, 0x1c000
	s_addc_u32 s19, s15, 0
	global_load_dwordx4 v[56:59], v208, s[18:19] sc1 nt
	s_add_u32 s18, s14, 0x1e000
	s_addc_u32 s19, s15, 0
	global_load_dwordx4 v[60:63], v208, s[18:19] sc1 nt
	s_waitcnt vmcnt(40)
	s_add_i32 s1, s20, 262
	s_lshr_b32 s2, s1, 10
	s_and_b32 s4, s1, 0x3ff
	s_lshr_b32 s5, s4, 6
	s_and_b32 s4, s4, 63
	s_lshl_b32 s12, s2, 22
	s_lshl_b32 s13, s4, 16
	s_add_i32 s12, s12, s13
	s_lshl_b32 s13, s5, 7
	s_add_i32 s12, s12, s13
	s_add_u32 s24, s90, s12
	s_addc_u32 s25, s91, 0
	s_add_u32 s24, s24, 0x3b100000
	s_addc_u32 s25, s25, 0
	s_add_u32 s26, s24, 0x1000
	s_addc_u32 s27, s25, 0
	v_pk_mul_f32 v[64:65], v[64:65], s[16:17] op_sel_hi:[1,0]
	v_pk_mul_f32 v[66:67], v[66:67], s[16:17] op_sel_hi:[1,0]
	v_pk_mul_f32 v[68:69], v[68:69], s[16:17] op_sel_hi:[1,0]
	v_pk_mul_f32 v[70:71], v[70:71], s[16:17] op_sel_hi:[1,0]
	v_pk_mul_f32 v[72:73], v[72:73], s[16:17] op_sel_hi:[1,0]
	v_pk_mul_f32 v[74:75], v[74:75], s[16:17] op_sel_hi:[1,0]
	v_pk_mul_f32 v[76:77], v[76:77], s[16:17] op_sel_hi:[1,0]
	v_pk_mul_f32 v[78:79], v[78:79], s[16:17] op_sel_hi:[1,0]
	v_pk_mul_f32 v[80:81], v[80:81], s[16:17] op_sel_hi:[1,0]
	v_pk_mul_f32 v[82:83], v[82:83], s[16:17] op_sel_hi:[1,0]
	v_pk_mul_f32 v[84:85], v[84:85], s[16:17] op_sel_hi:[1,0]
	v_pk_mul_f32 v[86:87], v[86:87], s[16:17] op_sel_hi:[1,0]
	v_pk_mul_f32 v[88:89], v[88:89], s[16:17] op_sel_hi:[1,0]
	v_pk_mul_f32 v[90:91], v[90:91], s[16:17] op_sel_hi:[1,0]
	v_pk_mul_f32 v[92:93], v[92:93], s[16:17] op_sel_hi:[1,0]
	v_pk_mul_f32 v[94:95], v[94:95], s[16:17] op_sel_hi:[1,0]
	v_pk_mul_f32 v[96:97], v[96:97], s[16:17] op_sel_hi:[1,0]
	v_pk_mul_f32 v[98:99], v[98:99], s[16:17] op_sel_hi:[1,0]
	v_pk_mul_f32 v[100:101], v[100:101], s[16:17] op_sel_hi:[1,0]
	v_pk_mul_f32 v[102:103], v[102:103], s[16:17] op_sel_hi:[1,0]
	v_pk_mul_f32 v[104:105], v[104:105], s[16:17] op_sel_hi:[1,0]
	v_pk_mul_f32 v[106:107], v[106:107], s[16:17] op_sel_hi:[1,0]
	v_pk_mul_f32 v[108:109], v[108:109], s[16:17] op_sel_hi:[1,0]
	v_pk_mul_f32 v[110:111], v[110:111], s[16:17] op_sel_hi:[1,0]
	v_pk_mul_f32 v[112:113], v[112:113], s[16:17] op_sel_hi:[1,0]
	v_pk_mul_f32 v[114:115], v[114:115], s[16:17] op_sel_hi:[1,0]
	v_pk_mul_f32 v[116:117], v[116:117], s[16:17] op_sel_hi:[1,0]
	v_pk_mul_f32 v[118:119], v[118:119], s[16:17] op_sel_hi:[1,0]
	v_pk_mul_f32 v[120:121], v[120:121], s[16:17] op_sel_hi:[1,0]
	v_pk_mul_f32 v[122:123], v[122:123], s[16:17] op_sel_hi:[1,0]
	v_pk_mul_f32 v[124:125], v[124:125], s[16:17] op_sel_hi:[1,0]
	v_pk_mul_f32 v[126:127], v[126:127], s[16:17] op_sel_hi:[1,0]
	v_cvt_pk_fp8_f32 v192, v64, v68
	v_cvt_pk_fp8_f32 v192, v72, v76 op_sel:[0,0,1]
	v_cvt_pk_fp8_f32 v193, v80, v84
	v_cvt_pk_fp8_f32 v193, v88, v92 op_sel:[0,0,1]
	v_cvt_pk_fp8_f32 v194, v96, v100
	v_cvt_pk_fp8_f32 v194, v104, v108 op_sel:[0,0,1]
	v_cvt_pk_fp8_f32 v195, v112, v116
	v_cvt_pk_fp8_f32 v195, v120, v124 op_sel:[0,0,1]
	global_store_dwordx4 v209, v[192:195], s[24:25] sc1
	v_cvt_pk_fp8_f32 v196, v65, v69
	v_cvt_pk_fp8_f32 v196, v73, v77 op_sel:[0,0,1]
	v_cvt_pk_fp8_f32 v197, v81, v85
	v_cvt_pk_fp8_f32 v197, v89, v93 op_sel:[0,0,1]
	v_cvt_pk_fp8_f32 v198, v97, v101
	v_cvt_pk_fp8_f32 v198, v105, v109 op_sel:[0,0,1]
	v_cvt_pk_fp8_f32 v199, v113, v117
	v_cvt_pk_fp8_f32 v199, v121, v125 op_sel:[0,0,1]
	global_store_dwordx4 v209, v[196:199], s[24:25] offset:2048 sc1
	v_cvt_pk_fp8_f32 v200, v66, v70
	v_cvt_pk_fp8_f32 v200, v74, v78 op_sel:[0,0,1]
	v_cvt_pk_fp8_f32 v201, v82, v86
	v_cvt_pk_fp8_f32 v201, v90, v94 op_sel:[0,0,1]
	v_cvt_pk_fp8_f32 v202, v98, v102
	v_cvt_pk_fp8_f32 v202, v106, v110 op_sel:[0,0,1]
	v_cvt_pk_fp8_f32 v203, v114, v118
	v_cvt_pk_fp8_f32 v203, v122, v126 op_sel:[0,0,1]
	global_store_dwordx4 v209, v[200:203], s[26:27] sc1
	v_cvt_pk_fp8_f32 v204, v67, v71
	v_cvt_pk_fp8_f32 v204, v75, v79 op_sel:[0,0,1]
	v_cvt_pk_fp8_f32 v205, v83, v87
	v_cvt_pk_fp8_f32 v205, v91, v95 op_sel:[0,0,1]
	v_cvt_pk_fp8_f32 v206, v99, v103
	v_cvt_pk_fp8_f32 v206, v107, v111 op_sel:[0,0,1]
	v_cvt_pk_fp8_f32 v207, v115, v119
	v_cvt_pk_fp8_f32 v207, v123, v127 op_sel:[0,0,1]
	global_store_dwordx4 v209, v[204:207], s[26:27] offset:2048 sc1
	s_add_i32 s1, s20, 10
	s_lshr_b32 s2, s1, 10
	s_and_b32 s4, s1, 0x3ff
	s_lshr_b32 s5, s4, 6
	s_and_b32 s4, s4, 63
	s_lshl_b32 s12, s2, 24
	s_lshl_b32 s13, s5, 20
	s_add_i32 s12, s12, s13
	s_lshl_b32 s13, s4, 7
	s_add_i32 s12, s12, s13
	s_add_u32 s14, s70, s12
	s_addc_u32 s15, s71, 0
	global_load_dwordx4 v[64:67], v208, s[14:15] sc1 nt
	s_add_u32 s18, s14, 0x2000
	s_addc_u32 s19, s15, 0
	global_load_dwordx4 v[68:71], v208, s[18:19] sc1 nt
	s_add_u32 s18, s14, 0x4000
	s_addc_u32 s19, s15, 0
	global_load_dwordx4 v[72:75], v208, s[18:19] sc1 nt
	s_add_u32 s18, s14, 0x6000
	s_addc_u32 s19, s15, 0
	global_load_dwordx4 v[76:79], v208, s[18:19] sc1 nt
	s_add_u32 s18, s14, 0x8000
	s_addc_u32 s19, s15, 0
	global_load_dwordx4 v[80:83], v208, s[18:19] sc1 nt
	s_add_u32 s18, s14, 0xa000
	s_addc_u32 s19, s15, 0
	global_load_dwordx4 v[84:87], v208, s[18:19] sc1 nt
	s_add_u32 s18, s14, 0xc000
	s_addc_u32 s19, s15, 0
	global_load_dwordx4 v[88:91], v208, s[18:19] sc1 nt
	s_add_u32 s18, s14, 0xe000
	s_addc_u32 s19, s15, 0
	global_load_dwordx4 v[92:95], v208, s[18:19] sc1 nt
	s_add_u32 s18, s14, 0x10000
	s_addc_u32 s19, s15, 0
	global_load_dwordx4 v[96:99], v208, s[18:19] sc1 nt
	s_add_u32 s18, s14, 0x12000
	s_addc_u32 s19, s15, 0
	global_load_dwordx4 v[100:103], v208, s[18:19] sc1 nt
	s_add_u32 s18, s14, 0x14000
	s_addc_u32 s19, s15, 0
	global_load_dwordx4 v[104:107], v208, s[18:19] sc1 nt
	s_add_u32 s18, s14, 0x16000
	s_addc_u32 s19, s15, 0
	global_load_dwordx4 v[108:111], v208, s[18:19] sc1 nt
	s_add_u32 s18, s14, 0x18000
	s_addc_u32 s19, s15, 0
	global_load_dwordx4 v[112:115], v208, s[18:19] sc1 nt
	s_add_u32 s18, s14, 0x1a000
	s_addc_u32 s19, s15, 0
	global_load_dwordx4 v[116:119], v208, s[18:19] sc1 nt
	s_add_u32 s18, s14, 0x1c000
	s_addc_u32 s19, s15, 0
	global_load_dwordx4 v[120:123], v208, s[18:19] sc1 nt
	s_add_u32 s18, s14, 0x1e000
	s_addc_u32 s19, s15, 0
	global_load_dwordx4 v[124:127], v208, s[18:19] sc1 nt
	s_waitcnt vmcnt(40)
	s_add_i32 s1, s20, 8
	s_lshr_b32 s2, s1, 10
	s_and_b32 s4, s1, 0x3ff
	s_lshr_b32 s5, s4, 6
	s_and_b32 s4, s4, 63
	s_lshl_b32 s12, s2, 22
	s_lshl_b32 s13, s4, 16
	s_add_i32 s12, s12, s13
	s_lshl_b32 s13, s5, 7
	s_add_i32 s12, s12, s13
	s_add_u32 s24, s90, s12
	s_addc_u32 s25, s91, 0
	s_add_u32 s24, s24, 0x3b100000
	s_addc_u32 s25, s25, 0
	s_add_u32 s26, s24, 0x1000
	s_addc_u32 s27, s25, 0
	v_pk_mul_f32 v[128:129], v[128:129], s[16:17] op_sel_hi:[1,0]
	v_pk_mul_f32 v[130:131], v[130:131], s[16:17] op_sel_hi:[1,0]
	v_pk_mul_f32 v[132:133], v[132:133], s[16:17] op_sel_hi:[1,0]
	v_pk_mul_f32 v[134:135], v[134:135], s[16:17] op_sel_hi:[1,0]
	v_pk_mul_f32 v[136:137], v[136:137], s[16:17] op_sel_hi:[1,0]
	v_pk_mul_f32 v[138:139], v[138:139], s[16:17] op_sel_hi:[1,0]
	v_pk_mul_f32 v[140:141], v[140:141], s[16:17] op_sel_hi:[1,0]
	v_pk_mul_f32 v[142:143], v[142:143], s[16:17] op_sel_hi:[1,0]
	v_pk_mul_f32 v[144:145], v[144:145], s[16:17] op_sel_hi:[1,0]
	v_pk_mul_f32 v[146:147], v[146:147], s[16:17] op_sel_hi:[1,0]
	v_pk_mul_f32 v[148:149], v[148:149], s[16:17] op_sel_hi:[1,0]
	v_pk_mul_f32 v[150:151], v[150:151], s[16:17] op_sel_hi:[1,0]
	v_pk_mul_f32 v[152:153], v[152:153], s[16:17] op_sel_hi:[1,0]
	v_pk_mul_f32 v[154:155], v[154:155], s[16:17] op_sel_hi:[1,0]
	v_pk_mul_f32 v[156:157], v[156:157], s[16:17] op_sel_hi:[1,0]
	v_pk_mul_f32 v[158:159], v[158:159], s[16:17] op_sel_hi:[1,0]
	v_pk_mul_f32 v[160:161], v[160:161], s[16:17] op_sel_hi:[1,0]
	v_pk_mul_f32 v[162:163], v[162:163], s[16:17] op_sel_hi:[1,0]
	v_pk_mul_f32 v[164:165], v[164:165], s[16:17] op_sel_hi:[1,0]
	v_pk_mul_f32 v[166:167], v[166:167], s[16:17] op_sel_hi:[1,0]
	v_pk_mul_f32 v[168:169], v[168:169], s[16:17] op_sel_hi:[1,0]
	v_pk_mul_f32 v[170:171], v[170:171], s[16:17] op_sel_hi:[1,0]
	v_pk_mul_f32 v[172:173], v[172:173], s[16:17] op_sel_hi:[1,0]
	v_pk_mul_f32 v[174:175], v[174:175], s[16:17] op_sel_hi:[1,0]
	v_pk_mul_f32 v[176:177], v[176:177], s[16:17] op_sel_hi:[1,0]
	v_pk_mul_f32 v[178:179], v[178:179], s[16:17] op_sel_hi:[1,0]
	v_pk_mul_f32 v[180:181], v[180:181], s[16:17] op_sel_hi:[1,0]
	v_pk_mul_f32 v[182:183], v[182:183], s[16:17] op_sel_hi:[1,0]
	v_pk_mul_f32 v[184:185], v[184:185], s[16:17] op_sel_hi:[1,0]
	v_pk_mul_f32 v[186:187], v[186:187], s[16:17] op_sel_hi:[1,0]
	v_pk_mul_f32 v[188:189], v[188:189], s[16:17] op_sel_hi:[1,0]
	v_pk_mul_f32 v[190:191], v[190:191], s[16:17] op_sel_hi:[1,0]
	v_cvt_pk_fp8_f32 v192, v128, v132
	v_cvt_pk_fp8_f32 v192, v136, v140 op_sel:[0,0,1]
	v_cvt_pk_fp8_f32 v193, v144, v148
	v_cvt_pk_fp8_f32 v193, v152, v156 op_sel:[0,0,1]
	v_cvt_pk_fp8_f32 v194, v160, v164
	v_cvt_pk_fp8_f32 v194, v168, v172 op_sel:[0,0,1]
	v_cvt_pk_fp8_f32 v195, v176, v180
	v_cvt_pk_fp8_f32 v195, v184, v188 op_sel:[0,0,1]
	global_store_dwordx4 v209, v[192:195], s[24:25] sc1
	v_cvt_pk_fp8_f32 v196, v129, v133
	v_cvt_pk_fp8_f32 v196, v137, v141 op_sel:[0,0,1]
	v_cvt_pk_fp8_f32 v197, v145, v149
	v_cvt_pk_fp8_f32 v197, v153, v157 op_sel:[0,0,1]
	v_cvt_pk_fp8_f32 v198, v161, v165
	v_cvt_pk_fp8_f32 v198, v169, v173 op_sel:[0,0,1]
	v_cvt_pk_fp8_f32 v199, v177, v181
	v_cvt_pk_fp8_f32 v199, v185, v189 op_sel:[0,0,1]
	global_store_dwordx4 v209, v[196:199], s[24:25] offset:2048 sc1
	v_cvt_pk_fp8_f32 v200, v130, v134
	v_cvt_pk_fp8_f32 v200, v138, v142 op_sel:[0,0,1]
	v_cvt_pk_fp8_f32 v201, v146, v150
	v_cvt_pk_fp8_f32 v201, v154, v158 op_sel:[0,0,1]
	v_cvt_pk_fp8_f32 v202, v162, v166
	v_cvt_pk_fp8_f32 v202, v170, v174 op_sel:[0,0,1]
	v_cvt_pk_fp8_f32 v203, v178, v182
	v_cvt_pk_fp8_f32 v203, v186, v190 op_sel:[0,0,1]
	global_store_dwordx4 v209, v[200:203], s[26:27] sc1
	v_cvt_pk_fp8_f32 v204, v131, v135
	v_cvt_pk_fp8_f32 v204, v139, v143 op_sel:[0,0,1]
	v_cvt_pk_fp8_f32 v205, v147, v151
	v_cvt_pk_fp8_f32 v205, v155, v159 op_sel:[0,0,1]
	v_cvt_pk_fp8_f32 v206, v163, v167
	v_cvt_pk_fp8_f32 v206, v171, v175 op_sel:[0,0,1]
	v_cvt_pk_fp8_f32 v207, v179, v183
	v_cvt_pk_fp8_f32 v207, v187, v191 op_sel:[0,0,1]
	global_store_dwordx4 v209, v[204:207], s[26:27] offset:2048 sc1
	s_add_i32 s1, s20, 266
	s_lshr_b32 s2, s1, 10
	s_and_b32 s4, s1, 0x3ff
	s_lshr_b32 s5, s4, 6
	s_and_b32 s4, s4, 63
	s_lshl_b32 s12, s2, 24
	s_lshl_b32 s13, s5, 20
	s_add_i32 s12, s12, s13
	s_lshl_b32 s13, s4, 7
	s_add_i32 s12, s12, s13
	s_add_u32 s14, s70, s12
	s_addc_u32 s15, s71, 0
	global_load_dwordx4 v[128:131], v208, s[14:15] sc1 nt
	s_add_u32 s18, s14, 0x2000
	s_addc_u32 s19, s15, 0
	global_load_dwordx4 v[132:135], v208, s[18:19] sc1 nt
	s_add_u32 s18, s14, 0x4000
	s_addc_u32 s19, s15, 0
	global_load_dwordx4 v[136:139], v208, s[18:19] sc1 nt
	s_add_u32 s18, s14, 0x6000
	s_addc_u32 s19, s15, 0
	global_load_dwordx4 v[140:143], v208, s[18:19] sc1 nt
	s_add_u32 s18, s14, 0x8000
	s_addc_u32 s19, s15, 0
	global_load_dwordx4 v[144:147], v208, s[18:19] sc1 nt
	s_add_u32 s18, s14, 0xa000
	s_addc_u32 s19, s15, 0
	global_load_dwordx4 v[148:151], v208, s[18:19] sc1 nt
	s_add_u32 s18, s14, 0xc000
	s_addc_u32 s19, s15, 0
	global_load_dwordx4 v[152:155], v208, s[18:19] sc1 nt
	s_add_u32 s18, s14, 0xe000
	s_addc_u32 s19, s15, 0
	global_load_dwordx4 v[156:159], v208, s[18:19] sc1 nt
	s_add_u32 s18, s14, 0x10000
	s_addc_u32 s19, s15, 0
	global_load_dwordx4 v[160:163], v208, s[18:19] sc1 nt
	s_add_u32 s18, s14, 0x12000
	s_addc_u32 s19, s15, 0
	global_load_dwordx4 v[164:167], v208, s[18:19] sc1 nt
	s_add_u32 s18, s14, 0x14000
	s_addc_u32 s19, s15, 0
	global_load_dwordx4 v[168:171], v208, s[18:19] sc1 nt
	s_add_u32 s18, s14, 0x16000
	s_addc_u32 s19, s15, 0
	global_load_dwordx4 v[172:175], v208, s[18:19] sc1 nt
	s_add_u32 s18, s14, 0x18000
	s_addc_u32 s19, s15, 0
	global_load_dwordx4 v[176:179], v208, s[18:19] sc1 nt
	s_add_u32 s18, s14, 0x1a000
	s_addc_u32 s19, s15, 0
	global_load_dwordx4 v[180:183], v208, s[18:19] sc1 nt
	s_add_u32 s18, s14, 0x1c000
	s_addc_u32 s19, s15, 0
	global_load_dwordx4 v[184:187], v208, s[18:19] sc1 nt
	s_add_u32 s18, s14, 0x1e000
	s_addc_u32 s19, s15, 0
	global_load_dwordx4 v[188:191], v208, s[18:19] sc1 nt
	s_waitcnt vmcnt(40)
	s_add_i32 s1, s20, 264
	s_lshr_b32 s2, s1, 10
	s_and_b32 s4, s1, 0x3ff
	s_lshr_b32 s5, s4, 6
	s_and_b32 s4, s4, 63
	s_lshl_b32 s12, s2, 22
	s_lshl_b32 s13, s4, 16
	s_add_i32 s12, s12, s13
	s_lshl_b32 s13, s5, 7
	s_add_i32 s12, s12, s13
	s_add_u32 s24, s90, s12
	s_addc_u32 s25, s91, 0
	s_add_u32 s24, s24, 0x3b100000
	s_addc_u32 s25, s25, 0
	s_add_u32 s26, s24, 0x1000
	s_addc_u32 s27, s25, 0
	v_pk_mul_f32 v[0:1], v[0:1], s[16:17] op_sel_hi:[1,0]
	v_pk_mul_f32 v[2:3], v[2:3], s[16:17] op_sel_hi:[1,0]
	v_pk_mul_f32 v[4:5], v[4:5], s[16:17] op_sel_hi:[1,0]
	v_pk_mul_f32 v[6:7], v[6:7], s[16:17] op_sel_hi:[1,0]
	v_pk_mul_f32 v[8:9], v[8:9], s[16:17] op_sel_hi:[1,0]
	v_pk_mul_f32 v[10:11], v[10:11], s[16:17] op_sel_hi:[1,0]
	v_pk_mul_f32 v[12:13], v[12:13], s[16:17] op_sel_hi:[1,0]
	v_pk_mul_f32 v[14:15], v[14:15], s[16:17] op_sel_hi:[1,0]
	v_pk_mul_f32 v[16:17], v[16:17], s[16:17] op_sel_hi:[1,0]
	v_pk_mul_f32 v[18:19], v[18:19], s[16:17] op_sel_hi:[1,0]
	v_pk_mul_f32 v[20:21], v[20:21], s[16:17] op_sel_hi:[1,0]
	v_pk_mul_f32 v[22:23], v[22:23], s[16:17] op_sel_hi:[1,0]
	v_pk_mul_f32 v[24:25], v[24:25], s[16:17] op_sel_hi:[1,0]
	v_pk_mul_f32 v[26:27], v[26:27], s[16:17] op_sel_hi:[1,0]
	v_pk_mul_f32 v[28:29], v[28:29], s[16:17] op_sel_hi:[1,0]
	v_pk_mul_f32 v[30:31], v[30:31], s[16:17] op_sel_hi:[1,0]
	v_pk_mul_f32 v[32:33], v[32:33], s[16:17] op_sel_hi:[1,0]
	v_pk_mul_f32 v[34:35], v[34:35], s[16:17] op_sel_hi:[1,0]
	v_pk_mul_f32 v[36:37], v[36:37], s[16:17] op_sel_hi:[1,0]
	v_pk_mul_f32 v[38:39], v[38:39], s[16:17] op_sel_hi:[1,0]
	v_pk_mul_f32 v[40:41], v[40:41], s[16:17] op_sel_hi:[1,0]
	v_pk_mul_f32 v[42:43], v[42:43], s[16:17] op_sel_hi:[1,0]
	v_pk_mul_f32 v[44:45], v[44:45], s[16:17] op_sel_hi:[1,0]
	v_pk_mul_f32 v[46:47], v[46:47], s[16:17] op_sel_hi:[1,0]
	v_pk_mul_f32 v[48:49], v[48:49], s[16:17] op_sel_hi:[1,0]
	v_pk_mul_f32 v[50:51], v[50:51], s[16:17] op_sel_hi:[1,0]
	v_pk_mul_f32 v[52:53], v[52:53], s[16:17] op_sel_hi:[1,0]
	v_pk_mul_f32 v[54:55], v[54:55], s[16:17] op_sel_hi:[1,0]
	v_pk_mul_f32 v[56:57], v[56:57], s[16:17] op_sel_hi:[1,0]
	v_pk_mul_f32 v[58:59], v[58:59], s[16:17] op_sel_hi:[1,0]
	v_pk_mul_f32 v[60:61], v[60:61], s[16:17] op_sel_hi:[1,0]
	v_pk_mul_f32 v[62:63], v[62:63], s[16:17] op_sel_hi:[1,0]
	v_cvt_pk_fp8_f32 v192, v0, v4
	v_cvt_pk_fp8_f32 v192, v8, v12 op_sel:[0,0,1]
	v_cvt_pk_fp8_f32 v193, v16, v20
	v_cvt_pk_fp8_f32 v193, v24, v28 op_sel:[0,0,1]
	v_cvt_pk_fp8_f32 v194, v32, v36
	v_cvt_pk_fp8_f32 v194, v40, v44 op_sel:[0,0,1]
	v_cvt_pk_fp8_f32 v195, v48, v52
	v_cvt_pk_fp8_f32 v195, v56, v60 op_sel:[0,0,1]
	global_store_dwordx4 v209, v[192:195], s[24:25] sc1
	v_cvt_pk_fp8_f32 v196, v1, v5
	v_cvt_pk_fp8_f32 v196, v9, v13 op_sel:[0,0,1]
	v_cvt_pk_fp8_f32 v197, v17, v21
	v_cvt_pk_fp8_f32 v197, v25, v29 op_sel:[0,0,1]
	v_cvt_pk_fp8_f32 v198, v33, v37
	v_cvt_pk_fp8_f32 v198, v41, v45 op_sel:[0,0,1]
	v_cvt_pk_fp8_f32 v199, v49, v53
	v_cvt_pk_fp8_f32 v199, v57, v61 op_sel:[0,0,1]
	global_store_dwordx4 v209, v[196:199], s[24:25] offset:2048 sc1
	v_cvt_pk_fp8_f32 v200, v2, v6
	v_cvt_pk_fp8_f32 v200, v10, v14 op_sel:[0,0,1]
	v_cvt_pk_fp8_f32 v201, v18, v22
	v_cvt_pk_fp8_f32 v201, v26, v30 op_sel:[0,0,1]
	v_cvt_pk_fp8_f32 v202, v34, v38
	v_cvt_pk_fp8_f32 v202, v42, v46 op_sel:[0,0,1]
	v_cvt_pk_fp8_f32 v203, v50, v54
	v_cvt_pk_fp8_f32 v203, v58, v62 op_sel:[0,0,1]
	global_store_dwordx4 v209, v[200:203], s[26:27] sc1
	v_cvt_pk_fp8_f32 v204, v3, v7
	v_cvt_pk_fp8_f32 v204, v11, v15 op_sel:[0,0,1]
	v_cvt_pk_fp8_f32 v205, v19, v23
	v_cvt_pk_fp8_f32 v205, v27, v31 op_sel:[0,0,1]
	v_cvt_pk_fp8_f32 v206, v35, v39
	v_cvt_pk_fp8_f32 v206, v43, v47 op_sel:[0,0,1]
	v_cvt_pk_fp8_f32 v207, v51, v55
	v_cvt_pk_fp8_f32 v207, v59, v63 op_sel:[0,0,1]
	global_store_dwordx4 v209, v[204:207], s[26:27] offset:2048 sc1
	s_add_i32 s1, s20, 12
	s_lshr_b32 s2, s1, 10
	s_and_b32 s4, s1, 0x3ff
	s_lshr_b32 s5, s4, 6
	s_and_b32 s4, s4, 63
	s_lshl_b32 s12, s2, 24
	s_lshl_b32 s13, s5, 20
	s_add_i32 s12, s12, s13
	s_lshl_b32 s13, s4, 7
	s_add_i32 s12, s12, s13
	s_add_u32 s14, s70, s12
	s_addc_u32 s15, s71, 0
	global_load_dwordx4 v[0:3], v208, s[14:15] sc1 nt
	s_add_u32 s18, s14, 0x2000
	s_addc_u32 s19, s15, 0
	global_load_dwordx4 v[4:7], v208, s[18:19] sc1 nt
	s_add_u32 s18, s14, 0x4000
	s_addc_u32 s19, s15, 0
	global_load_dwordx4 v[8:11], v208, s[18:19] sc1 nt
	s_add_u32 s18, s14, 0x6000
	s_addc_u32 s19, s15, 0
	global_load_dwordx4 v[12:15], v208, s[18:19] sc1 nt
	s_add_u32 s18, s14, 0x8000
	s_addc_u32 s19, s15, 0
	global_load_dwordx4 v[16:19], v208, s[18:19] sc1 nt
	s_add_u32 s18, s14, 0xa000
	s_addc_u32 s19, s15, 0
	global_load_dwordx4 v[20:23], v208, s[18:19] sc1 nt
	s_add_u32 s18, s14, 0xc000
	s_addc_u32 s19, s15, 0
	global_load_dwordx4 v[24:27], v208, s[18:19] sc1 nt
	s_add_u32 s18, s14, 0xe000
	s_addc_u32 s19, s15, 0
	global_load_dwordx4 v[28:31], v208, s[18:19] sc1 nt
	s_add_u32 s18, s14, 0x10000
	s_addc_u32 s19, s15, 0
	global_load_dwordx4 v[32:35], v208, s[18:19] sc1 nt
	s_add_u32 s18, s14, 0x12000
	s_addc_u32 s19, s15, 0
	global_load_dwordx4 v[36:39], v208, s[18:19] sc1 nt
	s_add_u32 s18, s14, 0x14000
	s_addc_u32 s19, s15, 0
	global_load_dwordx4 v[40:43], v208, s[18:19] sc1 nt
	s_add_u32 s18, s14, 0x16000
	s_addc_u32 s19, s15, 0
	global_load_dwordx4 v[44:47], v208, s[18:19] sc1 nt
	s_add_u32 s18, s14, 0x18000
	s_addc_u32 s19, s15, 0
	global_load_dwordx4 v[48:51], v208, s[18:19] sc1 nt
	s_add_u32 s18, s14, 0x1a000
	s_addc_u32 s19, s15, 0
	global_load_dwordx4 v[52:55], v208, s[18:19] sc1 nt
	s_add_u32 s18, s14, 0x1c000
	s_addc_u32 s19, s15, 0
	global_load_dwordx4 v[56:59], v208, s[18:19] sc1 nt
	s_add_u32 s18, s14, 0x1e000
	s_addc_u32 s19, s15, 0
	global_load_dwordx4 v[60:63], v208, s[18:19] sc1 nt
	s_waitcnt vmcnt(40)
	s_add_i32 s1, s20, 10
	s_lshr_b32 s2, s1, 10
	s_and_b32 s4, s1, 0x3ff
	s_lshr_b32 s5, s4, 6
	s_and_b32 s4, s4, 63
	s_lshl_b32 s12, s2, 22
	s_lshl_b32 s13, s4, 16
	s_add_i32 s12, s12, s13
	s_lshl_b32 s13, s5, 7
	s_add_i32 s12, s12, s13
	s_add_u32 s24, s90, s12
	s_addc_u32 s25, s91, 0
	s_add_u32 s24, s24, 0x3b100000
	s_addc_u32 s25, s25, 0
	s_add_u32 s26, s24, 0x1000
	s_addc_u32 s27, s25, 0
	v_pk_mul_f32 v[64:65], v[64:65], s[16:17] op_sel_hi:[1,0]
	v_pk_mul_f32 v[66:67], v[66:67], s[16:17] op_sel_hi:[1,0]
	v_pk_mul_f32 v[68:69], v[68:69], s[16:17] op_sel_hi:[1,0]
	v_pk_mul_f32 v[70:71], v[70:71], s[16:17] op_sel_hi:[1,0]
	v_pk_mul_f32 v[72:73], v[72:73], s[16:17] op_sel_hi:[1,0]
	v_pk_mul_f32 v[74:75], v[74:75], s[16:17] op_sel_hi:[1,0]
	v_pk_mul_f32 v[76:77], v[76:77], s[16:17] op_sel_hi:[1,0]
	v_pk_mul_f32 v[78:79], v[78:79], s[16:17] op_sel_hi:[1,0]
	v_pk_mul_f32 v[80:81], v[80:81], s[16:17] op_sel_hi:[1,0]
	v_pk_mul_f32 v[82:83], v[82:83], s[16:17] op_sel_hi:[1,0]
	v_pk_mul_f32 v[84:85], v[84:85], s[16:17] op_sel_hi:[1,0]
	v_pk_mul_f32 v[86:87], v[86:87], s[16:17] op_sel_hi:[1,0]
	v_pk_mul_f32 v[88:89], v[88:89], s[16:17] op_sel_hi:[1,0]
	v_pk_mul_f32 v[90:91], v[90:91], s[16:17] op_sel_hi:[1,0]
	v_pk_mul_f32 v[92:93], v[92:93], s[16:17] op_sel_hi:[1,0]
	v_pk_mul_f32 v[94:95], v[94:95], s[16:17] op_sel_hi:[1,0]
	v_pk_mul_f32 v[96:97], v[96:97], s[16:17] op_sel_hi:[1,0]
	v_pk_mul_f32 v[98:99], v[98:99], s[16:17] op_sel_hi:[1,0]
	v_pk_mul_f32 v[100:101], v[100:101], s[16:17] op_sel_hi:[1,0]
	v_pk_mul_f32 v[102:103], v[102:103], s[16:17] op_sel_hi:[1,0]
	v_pk_mul_f32 v[104:105], v[104:105], s[16:17] op_sel_hi:[1,0]
	v_pk_mul_f32 v[106:107], v[106:107], s[16:17] op_sel_hi:[1,0]
	v_pk_mul_f32 v[108:109], v[108:109], s[16:17] op_sel_hi:[1,0]
	v_pk_mul_f32 v[110:111], v[110:111], s[16:17] op_sel_hi:[1,0]
	v_pk_mul_f32 v[112:113], v[112:113], s[16:17] op_sel_hi:[1,0]
	v_pk_mul_f32 v[114:115], v[114:115], s[16:17] op_sel_hi:[1,0]
	v_pk_mul_f32 v[116:117], v[116:117], s[16:17] op_sel_hi:[1,0]
	v_pk_mul_f32 v[118:119], v[118:119], s[16:17] op_sel_hi:[1,0]
	v_pk_mul_f32 v[120:121], v[120:121], s[16:17] op_sel_hi:[1,0]
	v_pk_mul_f32 v[122:123], v[122:123], s[16:17] op_sel_hi:[1,0]
	v_pk_mul_f32 v[124:125], v[124:125], s[16:17] op_sel_hi:[1,0]
	v_pk_mul_f32 v[126:127], v[126:127], s[16:17] op_sel_hi:[1,0]
	v_cvt_pk_fp8_f32 v192, v64, v68
	v_cvt_pk_fp8_f32 v192, v72, v76 op_sel:[0,0,1]
	v_cvt_pk_fp8_f32 v193, v80, v84
	v_cvt_pk_fp8_f32 v193, v88, v92 op_sel:[0,0,1]
	v_cvt_pk_fp8_f32 v194, v96, v100
	v_cvt_pk_fp8_f32 v194, v104, v108 op_sel:[0,0,1]
	v_cvt_pk_fp8_f32 v195, v112, v116
	v_cvt_pk_fp8_f32 v195, v120, v124 op_sel:[0,0,1]
	global_store_dwordx4 v209, v[192:195], s[24:25] sc1
	v_cvt_pk_fp8_f32 v196, v65, v69
	v_cvt_pk_fp8_f32 v196, v73, v77 op_sel:[0,0,1]
	v_cvt_pk_fp8_f32 v197, v81, v85
	v_cvt_pk_fp8_f32 v197, v89, v93 op_sel:[0,0,1]
	v_cvt_pk_fp8_f32 v198, v97, v101
	v_cvt_pk_fp8_f32 v198, v105, v109 op_sel:[0,0,1]
	v_cvt_pk_fp8_f32 v199, v113, v117
	v_cvt_pk_fp8_f32 v199, v121, v125 op_sel:[0,0,1]
	global_store_dwordx4 v209, v[196:199], s[24:25] offset:2048 sc1
	v_cvt_pk_fp8_f32 v200, v66, v70
	v_cvt_pk_fp8_f32 v200, v74, v78 op_sel:[0,0,1]
	v_cvt_pk_fp8_f32 v201, v82, v86
	v_cvt_pk_fp8_f32 v201, v90, v94 op_sel:[0,0,1]
	v_cvt_pk_fp8_f32 v202, v98, v102
	v_cvt_pk_fp8_f32 v202, v106, v110 op_sel:[0,0,1]
	v_cvt_pk_fp8_f32 v203, v114, v118
	v_cvt_pk_fp8_f32 v203, v122, v126 op_sel:[0,0,1]
	global_store_dwordx4 v209, v[200:203], s[26:27] sc1
	v_cvt_pk_fp8_f32 v204, v67, v71
	v_cvt_pk_fp8_f32 v204, v75, v79 op_sel:[0,0,1]
	v_cvt_pk_fp8_f32 v205, v83, v87
	v_cvt_pk_fp8_f32 v205, v91, v95 op_sel:[0,0,1]
	v_cvt_pk_fp8_f32 v206, v99, v103
	v_cvt_pk_fp8_f32 v206, v107, v111 op_sel:[0,0,1]
	v_cvt_pk_fp8_f32 v207, v115, v119
	v_cvt_pk_fp8_f32 v207, v123, v127 op_sel:[0,0,1]
	global_store_dwordx4 v209, v[204:207], s[26:27] offset:2048 sc1
	s_add_i32 s1, s20, 268
	s_lshr_b32 s2, s1, 10
	s_and_b32 s4, s1, 0x3ff
	s_lshr_b32 s5, s4, 6
	s_and_b32 s4, s4, 63
	s_lshl_b32 s12, s2, 24
	s_lshl_b32 s13, s5, 20
	s_add_i32 s12, s12, s13
	s_lshl_b32 s13, s4, 7
	s_add_i32 s12, s12, s13
	s_add_u32 s14, s70, s12
	s_addc_u32 s15, s71, 0
	global_load_dwordx4 v[64:67], v208, s[14:15] sc1 nt
	s_add_u32 s18, s14, 0x2000
	s_addc_u32 s19, s15, 0
	global_load_dwordx4 v[68:71], v208, s[18:19] sc1 nt
	s_add_u32 s18, s14, 0x4000
	s_addc_u32 s19, s15, 0
	global_load_dwordx4 v[72:75], v208, s[18:19] sc1 nt
	s_add_u32 s18, s14, 0x6000
	s_addc_u32 s19, s15, 0
	global_load_dwordx4 v[76:79], v208, s[18:19] sc1 nt
	s_add_u32 s18, s14, 0x8000
	s_addc_u32 s19, s15, 0
	global_load_dwordx4 v[80:83], v208, s[18:19] sc1 nt
	s_add_u32 s18, s14, 0xa000
	s_addc_u32 s19, s15, 0
	global_load_dwordx4 v[84:87], v208, s[18:19] sc1 nt
	s_add_u32 s18, s14, 0xc000
	s_addc_u32 s19, s15, 0
	global_load_dwordx4 v[88:91], v208, s[18:19] sc1 nt
	s_add_u32 s18, s14, 0xe000
	s_addc_u32 s19, s15, 0
	global_load_dwordx4 v[92:95], v208, s[18:19] sc1 nt
	s_add_u32 s18, s14, 0x10000
	s_addc_u32 s19, s15, 0
	global_load_dwordx4 v[96:99], v208, s[18:19] sc1 nt
	s_add_u32 s18, s14, 0x12000
	s_addc_u32 s19, s15, 0
	global_load_dwordx4 v[100:103], v208, s[18:19] sc1 nt
	s_add_u32 s18, s14, 0x14000
	s_addc_u32 s19, s15, 0
	global_load_dwordx4 v[104:107], v208, s[18:19] sc1 nt
	s_add_u32 s18, s14, 0x16000
	s_addc_u32 s19, s15, 0
	global_load_dwordx4 v[108:111], v208, s[18:19] sc1 nt
	s_add_u32 s18, s14, 0x18000
	s_addc_u32 s19, s15, 0
	global_load_dwordx4 v[112:115], v208, s[18:19] sc1 nt
	s_add_u32 s18, s14, 0x1a000
	s_addc_u32 s19, s15, 0
	global_load_dwordx4 v[116:119], v208, s[18:19] sc1 nt
	s_add_u32 s18, s14, 0x1c000
	s_addc_u32 s19, s15, 0
	global_load_dwordx4 v[120:123], v208, s[18:19] sc1 nt
	s_add_u32 s18, s14, 0x1e000
	s_addc_u32 s19, s15, 0
	global_load_dwordx4 v[124:127], v208, s[18:19] sc1 nt
	s_waitcnt vmcnt(40)
	s_add_i32 s1, s20, 266
	s_lshr_b32 s2, s1, 10
	s_and_b32 s4, s1, 0x3ff
	s_lshr_b32 s5, s4, 6
	s_and_b32 s4, s4, 63
	s_lshl_b32 s12, s2, 22
	s_lshl_b32 s13, s4, 16
	s_add_i32 s12, s12, s13
	s_lshl_b32 s13, s5, 7
	s_add_i32 s12, s12, s13
	s_add_u32 s24, s90, s12
	s_addc_u32 s25, s91, 0
	s_add_u32 s24, s24, 0x3b100000
	s_addc_u32 s25, s25, 0
	s_add_u32 s26, s24, 0x1000
	s_addc_u32 s27, s25, 0
	v_pk_mul_f32 v[128:129], v[128:129], s[16:17] op_sel_hi:[1,0]
	v_pk_mul_f32 v[130:131], v[130:131], s[16:17] op_sel_hi:[1,0]
	v_pk_mul_f32 v[132:133], v[132:133], s[16:17] op_sel_hi:[1,0]
	v_pk_mul_f32 v[134:135], v[134:135], s[16:17] op_sel_hi:[1,0]
	v_pk_mul_f32 v[136:137], v[136:137], s[16:17] op_sel_hi:[1,0]
	v_pk_mul_f32 v[138:139], v[138:139], s[16:17] op_sel_hi:[1,0]
	v_pk_mul_f32 v[140:141], v[140:141], s[16:17] op_sel_hi:[1,0]
	v_pk_mul_f32 v[142:143], v[142:143], s[16:17] op_sel_hi:[1,0]
	v_pk_mul_f32 v[144:145], v[144:145], s[16:17] op_sel_hi:[1,0]
	v_pk_mul_f32 v[146:147], v[146:147], s[16:17] op_sel_hi:[1,0]
	v_pk_mul_f32 v[148:149], v[148:149], s[16:17] op_sel_hi:[1,0]
	v_pk_mul_f32 v[150:151], v[150:151], s[16:17] op_sel_hi:[1,0]
	v_pk_mul_f32 v[152:153], v[152:153], s[16:17] op_sel_hi:[1,0]
	v_pk_mul_f32 v[154:155], v[154:155], s[16:17] op_sel_hi:[1,0]
	v_pk_mul_f32 v[156:157], v[156:157], s[16:17] op_sel_hi:[1,0]
	v_pk_mul_f32 v[158:159], v[158:159], s[16:17] op_sel_hi:[1,0]
	v_pk_mul_f32 v[160:161], v[160:161], s[16:17] op_sel_hi:[1,0]
	v_pk_mul_f32 v[162:163], v[162:163], s[16:17] op_sel_hi:[1,0]
	v_pk_mul_f32 v[164:165], v[164:165], s[16:17] op_sel_hi:[1,0]
	v_pk_mul_f32 v[166:167], v[166:167], s[16:17] op_sel_hi:[1,0]
	v_pk_mul_f32 v[168:169], v[168:169], s[16:17] op_sel_hi:[1,0]
	v_pk_mul_f32 v[170:171], v[170:171], s[16:17] op_sel_hi:[1,0]
	v_pk_mul_f32 v[172:173], v[172:173], s[16:17] op_sel_hi:[1,0]
	v_pk_mul_f32 v[174:175], v[174:175], s[16:17] op_sel_hi:[1,0]
	v_pk_mul_f32 v[176:177], v[176:177], s[16:17] op_sel_hi:[1,0]
	v_pk_mul_f32 v[178:179], v[178:179], s[16:17] op_sel_hi:[1,0]
	v_pk_mul_f32 v[180:181], v[180:181], s[16:17] op_sel_hi:[1,0]
	v_pk_mul_f32 v[182:183], v[182:183], s[16:17] op_sel_hi:[1,0]
	v_pk_mul_f32 v[184:185], v[184:185], s[16:17] op_sel_hi:[1,0]
	v_pk_mul_f32 v[186:187], v[186:187], s[16:17] op_sel_hi:[1,0]
	v_pk_mul_f32 v[188:189], v[188:189], s[16:17] op_sel_hi:[1,0]
	v_pk_mul_f32 v[190:191], v[190:191], s[16:17] op_sel_hi:[1,0]
	v_cvt_pk_fp8_f32 v192, v128, v132
	v_cvt_pk_fp8_f32 v192, v136, v140 op_sel:[0,0,1]
	v_cvt_pk_fp8_f32 v193, v144, v148
	v_cvt_pk_fp8_f32 v193, v152, v156 op_sel:[0,0,1]
	v_cvt_pk_fp8_f32 v194, v160, v164
	v_cvt_pk_fp8_f32 v194, v168, v172 op_sel:[0,0,1]
	v_cvt_pk_fp8_f32 v195, v176, v180
	v_cvt_pk_fp8_f32 v195, v184, v188 op_sel:[0,0,1]
	global_store_dwordx4 v209, v[192:195], s[24:25] sc1
	v_cvt_pk_fp8_f32 v196, v129, v133
	v_cvt_pk_fp8_f32 v196, v137, v141 op_sel:[0,0,1]
	v_cvt_pk_fp8_f32 v197, v145, v149
	v_cvt_pk_fp8_f32 v197, v153, v157 op_sel:[0,0,1]
	v_cvt_pk_fp8_f32 v198, v161, v165
	v_cvt_pk_fp8_f32 v198, v169, v173 op_sel:[0,0,1]
	v_cvt_pk_fp8_f32 v199, v177, v181
	v_cvt_pk_fp8_f32 v199, v185, v189 op_sel:[0,0,1]
	global_store_dwordx4 v209, v[196:199], s[24:25] offset:2048 sc1
	v_cvt_pk_fp8_f32 v200, v130, v134
	v_cvt_pk_fp8_f32 v200, v138, v142 op_sel:[0,0,1]
	v_cvt_pk_fp8_f32 v201, v146, v150
	v_cvt_pk_fp8_f32 v201, v154, v158 op_sel:[0,0,1]
	v_cvt_pk_fp8_f32 v202, v162, v166
	v_cvt_pk_fp8_f32 v202, v170, v174 op_sel:[0,0,1]
	v_cvt_pk_fp8_f32 v203, v178, v182
	v_cvt_pk_fp8_f32 v203, v186, v190 op_sel:[0,0,1]
	global_store_dwordx4 v209, v[200:203], s[26:27] sc1
	v_cvt_pk_fp8_f32 v204, v131, v135
	v_cvt_pk_fp8_f32 v204, v139, v143 op_sel:[0,0,1]
	v_cvt_pk_fp8_f32 v205, v147, v151
	v_cvt_pk_fp8_f32 v205, v155, v159 op_sel:[0,0,1]
	v_cvt_pk_fp8_f32 v206, v163, v167
	v_cvt_pk_fp8_f32 v206, v171, v175 op_sel:[0,0,1]
	v_cvt_pk_fp8_f32 v207, v179, v183
	v_cvt_pk_fp8_f32 v207, v187, v191 op_sel:[0,0,1]
	global_store_dwordx4 v209, v[204:207], s[26:27] offset:2048 sc1
	s_add_i32 s1, s20, 14
	s_lshr_b32 s2, s1, 10
	s_and_b32 s4, s1, 0x3ff
	s_lshr_b32 s5, s4, 6
	s_and_b32 s4, s4, 63
	s_lshl_b32 s12, s2, 24
	s_lshl_b32 s13, s5, 20
	s_add_i32 s12, s12, s13
	s_lshl_b32 s13, s4, 7
	s_add_i32 s12, s12, s13
	s_add_u32 s14, s70, s12
	s_addc_u32 s15, s71, 0
	global_load_dwordx4 v[128:131], v208, s[14:15] sc1 nt
	s_add_u32 s18, s14, 0x2000
	s_addc_u32 s19, s15, 0
	global_load_dwordx4 v[132:135], v208, s[18:19] sc1 nt
	s_add_u32 s18, s14, 0x4000
	s_addc_u32 s19, s15, 0
	global_load_dwordx4 v[136:139], v208, s[18:19] sc1 nt
	s_add_u32 s18, s14, 0x6000
	s_addc_u32 s19, s15, 0
	global_load_dwordx4 v[140:143], v208, s[18:19] sc1 nt
	s_add_u32 s18, s14, 0x8000
	s_addc_u32 s19, s15, 0
	global_load_dwordx4 v[144:147], v208, s[18:19] sc1 nt
	s_add_u32 s18, s14, 0xa000
	s_addc_u32 s19, s15, 0
	global_load_dwordx4 v[148:151], v208, s[18:19] sc1 nt
	s_add_u32 s18, s14, 0xc000
	s_addc_u32 s19, s15, 0
	global_load_dwordx4 v[152:155], v208, s[18:19] sc1 nt
	s_add_u32 s18, s14, 0xe000
	s_addc_u32 s19, s15, 0
	global_load_dwordx4 v[156:159], v208, s[18:19] sc1 nt
	s_add_u32 s18, s14, 0x10000
	s_addc_u32 s19, s15, 0
	global_load_dwordx4 v[160:163], v208, s[18:19] sc1 nt
	s_add_u32 s18, s14, 0x12000
	s_addc_u32 s19, s15, 0
	global_load_dwordx4 v[164:167], v208, s[18:19] sc1 nt
	s_add_u32 s18, s14, 0x14000
	s_addc_u32 s19, s15, 0
	global_load_dwordx4 v[168:171], v208, s[18:19] sc1 nt
	s_add_u32 s18, s14, 0x16000
	s_addc_u32 s19, s15, 0
	global_load_dwordx4 v[172:175], v208, s[18:19] sc1 nt
	s_add_u32 s18, s14, 0x18000
	s_addc_u32 s19, s15, 0
	global_load_dwordx4 v[176:179], v208, s[18:19] sc1 nt
	s_add_u32 s18, s14, 0x1a000
	s_addc_u32 s19, s15, 0
	global_load_dwordx4 v[180:183], v208, s[18:19] sc1 nt
	s_add_u32 s18, s14, 0x1c000
	s_addc_u32 s19, s15, 0
	global_load_dwordx4 v[184:187], v208, s[18:19] sc1 nt
	s_add_u32 s18, s14, 0x1e000
	s_addc_u32 s19, s15, 0
	global_load_dwordx4 v[188:191], v208, s[18:19] sc1 nt
	s_waitcnt vmcnt(40)
	s_add_i32 s1, s20, 12
	s_lshr_b32 s2, s1, 10
	s_and_b32 s4, s1, 0x3ff
	s_lshr_b32 s5, s4, 6
	s_and_b32 s4, s4, 63
	s_lshl_b32 s12, s2, 22
	s_lshl_b32 s13, s4, 16
	s_add_i32 s12, s12, s13
	s_lshl_b32 s13, s5, 7
	s_add_i32 s12, s12, s13
	s_add_u32 s24, s90, s12
	s_addc_u32 s25, s91, 0
	s_add_u32 s24, s24, 0x3b100000
	s_addc_u32 s25, s25, 0
	s_add_u32 s26, s24, 0x1000
	s_addc_u32 s27, s25, 0
	v_pk_mul_f32 v[0:1], v[0:1], s[16:17] op_sel_hi:[1,0]
	v_pk_mul_f32 v[2:3], v[2:3], s[16:17] op_sel_hi:[1,0]
	v_pk_mul_f32 v[4:5], v[4:5], s[16:17] op_sel_hi:[1,0]
	v_pk_mul_f32 v[6:7], v[6:7], s[16:17] op_sel_hi:[1,0]
	v_pk_mul_f32 v[8:9], v[8:9], s[16:17] op_sel_hi:[1,0]
	v_pk_mul_f32 v[10:11], v[10:11], s[16:17] op_sel_hi:[1,0]
	v_pk_mul_f32 v[12:13], v[12:13], s[16:17] op_sel_hi:[1,0]
	v_pk_mul_f32 v[14:15], v[14:15], s[16:17] op_sel_hi:[1,0]
	v_pk_mul_f32 v[16:17], v[16:17], s[16:17] op_sel_hi:[1,0]
	v_pk_mul_f32 v[18:19], v[18:19], s[16:17] op_sel_hi:[1,0]
	v_pk_mul_f32 v[20:21], v[20:21], s[16:17] op_sel_hi:[1,0]
	v_pk_mul_f32 v[22:23], v[22:23], s[16:17] op_sel_hi:[1,0]
	v_pk_mul_f32 v[24:25], v[24:25], s[16:17] op_sel_hi:[1,0]
	v_pk_mul_f32 v[26:27], v[26:27], s[16:17] op_sel_hi:[1,0]
	v_pk_mul_f32 v[28:29], v[28:29], s[16:17] op_sel_hi:[1,0]
	v_pk_mul_f32 v[30:31], v[30:31], s[16:17] op_sel_hi:[1,0]
	v_pk_mul_f32 v[32:33], v[32:33], s[16:17] op_sel_hi:[1,0]
	v_pk_mul_f32 v[34:35], v[34:35], s[16:17] op_sel_hi:[1,0]
	v_pk_mul_f32 v[36:37], v[36:37], s[16:17] op_sel_hi:[1,0]
	v_pk_mul_f32 v[38:39], v[38:39], s[16:17] op_sel_hi:[1,0]
	v_pk_mul_f32 v[40:41], v[40:41], s[16:17] op_sel_hi:[1,0]
	v_pk_mul_f32 v[42:43], v[42:43], s[16:17] op_sel_hi:[1,0]
	v_pk_mul_f32 v[44:45], v[44:45], s[16:17] op_sel_hi:[1,0]
	v_pk_mul_f32 v[46:47], v[46:47], s[16:17] op_sel_hi:[1,0]
	v_pk_mul_f32 v[48:49], v[48:49], s[16:17] op_sel_hi:[1,0]
	v_pk_mul_f32 v[50:51], v[50:51], s[16:17] op_sel_hi:[1,0]
	v_pk_mul_f32 v[52:53], v[52:53], s[16:17] op_sel_hi:[1,0]
	v_pk_mul_f32 v[54:55], v[54:55], s[16:17] op_sel_hi:[1,0]
	v_pk_mul_f32 v[56:57], v[56:57], s[16:17] op_sel_hi:[1,0]
	v_pk_mul_f32 v[58:59], v[58:59], s[16:17] op_sel_hi:[1,0]
	v_pk_mul_f32 v[60:61], v[60:61], s[16:17] op_sel_hi:[1,0]
	v_pk_mul_f32 v[62:63], v[62:63], s[16:17] op_sel_hi:[1,0]
	v_cvt_pk_fp8_f32 v192, v0, v4
	v_cvt_pk_fp8_f32 v192, v8, v12 op_sel:[0,0,1]
	v_cvt_pk_fp8_f32 v193, v16, v20
	v_cvt_pk_fp8_f32 v193, v24, v28 op_sel:[0,0,1]
	v_cvt_pk_fp8_f32 v194, v32, v36
	v_cvt_pk_fp8_f32 v194, v40, v44 op_sel:[0,0,1]
	v_cvt_pk_fp8_f32 v195, v48, v52
	v_cvt_pk_fp8_f32 v195, v56, v60 op_sel:[0,0,1]
	global_store_dwordx4 v209, v[192:195], s[24:25] sc1
	v_cvt_pk_fp8_f32 v196, v1, v5
	v_cvt_pk_fp8_f32 v196, v9, v13 op_sel:[0,0,1]
	v_cvt_pk_fp8_f32 v197, v17, v21
	v_cvt_pk_fp8_f32 v197, v25, v29 op_sel:[0,0,1]
	v_cvt_pk_fp8_f32 v198, v33, v37
	v_cvt_pk_fp8_f32 v198, v41, v45 op_sel:[0,0,1]
	v_cvt_pk_fp8_f32 v199, v49, v53
	v_cvt_pk_fp8_f32 v199, v57, v61 op_sel:[0,0,1]
	global_store_dwordx4 v209, v[196:199], s[24:25] offset:2048 sc1
	v_cvt_pk_fp8_f32 v200, v2, v6
	v_cvt_pk_fp8_f32 v200, v10, v14 op_sel:[0,0,1]
	v_cvt_pk_fp8_f32 v201, v18, v22
	v_cvt_pk_fp8_f32 v201, v26, v30 op_sel:[0,0,1]
	v_cvt_pk_fp8_f32 v202, v34, v38
	v_cvt_pk_fp8_f32 v202, v42, v46 op_sel:[0,0,1]
	v_cvt_pk_fp8_f32 v203, v50, v54
	v_cvt_pk_fp8_f32 v203, v58, v62 op_sel:[0,0,1]
	global_store_dwordx4 v209, v[200:203], s[26:27] sc1
	v_cvt_pk_fp8_f32 v204, v3, v7
	v_cvt_pk_fp8_f32 v204, v11, v15 op_sel:[0,0,1]
	v_cvt_pk_fp8_f32 v205, v19, v23
	v_cvt_pk_fp8_f32 v205, v27, v31 op_sel:[0,0,1]
	v_cvt_pk_fp8_f32 v206, v35, v39
	v_cvt_pk_fp8_f32 v206, v43, v47 op_sel:[0,0,1]
	v_cvt_pk_fp8_f32 v207, v51, v55
	v_cvt_pk_fp8_f32 v207, v59, v63 op_sel:[0,0,1]
	global_store_dwordx4 v209, v[204:207], s[26:27] offset:2048 sc1
	s_add_i32 s1, s20, 270
	s_lshr_b32 s2, s1, 10
	s_and_b32 s4, s1, 0x3ff
	s_lshr_b32 s5, s4, 6
	s_and_b32 s4, s4, 63
	s_lshl_b32 s12, s2, 24
	s_lshl_b32 s13, s5, 20
	s_add_i32 s12, s12, s13
	s_lshl_b32 s13, s4, 7
	s_add_i32 s12, s12, s13
	s_add_u32 s14, s70, s12
	s_addc_u32 s15, s71, 0
	global_load_dwordx4 v[0:3], v208, s[14:15] sc1 nt
	s_add_u32 s18, s14, 0x2000
	s_addc_u32 s19, s15, 0
	global_load_dwordx4 v[4:7], v208, s[18:19] sc1 nt
	s_add_u32 s18, s14, 0x4000
	s_addc_u32 s19, s15, 0
	global_load_dwordx4 v[8:11], v208, s[18:19] sc1 nt
	s_add_u32 s18, s14, 0x6000
	s_addc_u32 s19, s15, 0
	global_load_dwordx4 v[12:15], v208, s[18:19] sc1 nt
	s_add_u32 s18, s14, 0x8000
	s_addc_u32 s19, s15, 0
	global_load_dwordx4 v[16:19], v208, s[18:19] sc1 nt
	s_add_u32 s18, s14, 0xa000
	s_addc_u32 s19, s15, 0
	global_load_dwordx4 v[20:23], v208, s[18:19] sc1 nt
	s_add_u32 s18, s14, 0xc000
	s_addc_u32 s19, s15, 0
	global_load_dwordx4 v[24:27], v208, s[18:19] sc1 nt
	s_add_u32 s18, s14, 0xe000
	s_addc_u32 s19, s15, 0
	global_load_dwordx4 v[28:31], v208, s[18:19] sc1 nt
	s_add_u32 s18, s14, 0x10000
	s_addc_u32 s19, s15, 0
	global_load_dwordx4 v[32:35], v208, s[18:19] sc1 nt
	s_add_u32 s18, s14, 0x12000
	s_addc_u32 s19, s15, 0
	global_load_dwordx4 v[36:39], v208, s[18:19] sc1 nt
	s_add_u32 s18, s14, 0x14000
	s_addc_u32 s19, s15, 0
	global_load_dwordx4 v[40:43], v208, s[18:19] sc1 nt
	s_add_u32 s18, s14, 0x16000
	s_addc_u32 s19, s15, 0
	global_load_dwordx4 v[44:47], v208, s[18:19] sc1 nt
	s_add_u32 s18, s14, 0x18000
	s_addc_u32 s19, s15, 0
	global_load_dwordx4 v[48:51], v208, s[18:19] sc1 nt
	s_add_u32 s18, s14, 0x1a000
	s_addc_u32 s19, s15, 0
	global_load_dwordx4 v[52:55], v208, s[18:19] sc1 nt
	s_add_u32 s18, s14, 0x1c000
	s_addc_u32 s19, s15, 0
	global_load_dwordx4 v[56:59], v208, s[18:19] sc1 nt
	s_add_u32 s18, s14, 0x1e000
	s_addc_u32 s19, s15, 0
	global_load_dwordx4 v[60:63], v208, s[18:19] sc1 nt
	s_waitcnt vmcnt(40)
	s_add_i32 s1, s20, 268
	s_lshr_b32 s2, s1, 10
	s_and_b32 s4, s1, 0x3ff
	s_lshr_b32 s5, s4, 6
	s_and_b32 s4, s4, 63
	s_lshl_b32 s12, s2, 22
	s_lshl_b32 s13, s4, 16
	s_add_i32 s12, s12, s13
	s_lshl_b32 s13, s5, 7
	s_add_i32 s12, s12, s13
	s_add_u32 s24, s90, s12
	s_addc_u32 s25, s91, 0
	s_add_u32 s24, s24, 0x3b100000
	s_addc_u32 s25, s25, 0
	s_add_u32 s26, s24, 0x1000
	s_addc_u32 s27, s25, 0
	v_pk_mul_f32 v[64:65], v[64:65], s[16:17] op_sel_hi:[1,0]
	v_pk_mul_f32 v[66:67], v[66:67], s[16:17] op_sel_hi:[1,0]
	v_pk_mul_f32 v[68:69], v[68:69], s[16:17] op_sel_hi:[1,0]
	v_pk_mul_f32 v[70:71], v[70:71], s[16:17] op_sel_hi:[1,0]
	v_pk_mul_f32 v[72:73], v[72:73], s[16:17] op_sel_hi:[1,0]
	v_pk_mul_f32 v[74:75], v[74:75], s[16:17] op_sel_hi:[1,0]
	v_pk_mul_f32 v[76:77], v[76:77], s[16:17] op_sel_hi:[1,0]
	v_pk_mul_f32 v[78:79], v[78:79], s[16:17] op_sel_hi:[1,0]
	v_pk_mul_f32 v[80:81], v[80:81], s[16:17] op_sel_hi:[1,0]
	v_pk_mul_f32 v[82:83], v[82:83], s[16:17] op_sel_hi:[1,0]
	v_pk_mul_f32 v[84:85], v[84:85], s[16:17] op_sel_hi:[1,0]
	v_pk_mul_f32 v[86:87], v[86:87], s[16:17] op_sel_hi:[1,0]
	v_pk_mul_f32 v[88:89], v[88:89], s[16:17] op_sel_hi:[1,0]
	v_pk_mul_f32 v[90:91], v[90:91], s[16:17] op_sel_hi:[1,0]
	v_pk_mul_f32 v[92:93], v[92:93], s[16:17] op_sel_hi:[1,0]
	v_pk_mul_f32 v[94:95], v[94:95], s[16:17] op_sel_hi:[1,0]
	v_pk_mul_f32 v[96:97], v[96:97], s[16:17] op_sel_hi:[1,0]
	v_pk_mul_f32 v[98:99], v[98:99], s[16:17] op_sel_hi:[1,0]
	v_pk_mul_f32 v[100:101], v[100:101], s[16:17] op_sel_hi:[1,0]
	v_pk_mul_f32 v[102:103], v[102:103], s[16:17] op_sel_hi:[1,0]
	v_pk_mul_f32 v[104:105], v[104:105], s[16:17] op_sel_hi:[1,0]
	v_pk_mul_f32 v[106:107], v[106:107], s[16:17] op_sel_hi:[1,0]
	v_pk_mul_f32 v[108:109], v[108:109], s[16:17] op_sel_hi:[1,0]
	v_pk_mul_f32 v[110:111], v[110:111], s[16:17] op_sel_hi:[1,0]
	v_pk_mul_f32 v[112:113], v[112:113], s[16:17] op_sel_hi:[1,0]
	v_pk_mul_f32 v[114:115], v[114:115], s[16:17] op_sel_hi:[1,0]
	v_pk_mul_f32 v[116:117], v[116:117], s[16:17] op_sel_hi:[1,0]
	v_pk_mul_f32 v[118:119], v[118:119], s[16:17] op_sel_hi:[1,0]
	v_pk_mul_f32 v[120:121], v[120:121], s[16:17] op_sel_hi:[1,0]
	v_pk_mul_f32 v[122:123], v[122:123], s[16:17] op_sel_hi:[1,0]
	v_pk_mul_f32 v[124:125], v[124:125], s[16:17] op_sel_hi:[1,0]
	v_pk_mul_f32 v[126:127], v[126:127], s[16:17] op_sel_hi:[1,0]
	v_cvt_pk_fp8_f32 v192, v64, v68
	v_cvt_pk_fp8_f32 v192, v72, v76 op_sel:[0,0,1]
	v_cvt_pk_fp8_f32 v193, v80, v84
	v_cvt_pk_fp8_f32 v193, v88, v92 op_sel:[0,0,1]
	v_cvt_pk_fp8_f32 v194, v96, v100
	v_cvt_pk_fp8_f32 v194, v104, v108 op_sel:[0,0,1]
	v_cvt_pk_fp8_f32 v195, v112, v116
	v_cvt_pk_fp8_f32 v195, v120, v124 op_sel:[0,0,1]
	global_store_dwordx4 v209, v[192:195], s[24:25] sc1
	v_cvt_pk_fp8_f32 v196, v65, v69
	v_cvt_pk_fp8_f32 v196, v73, v77 op_sel:[0,0,1]
	v_cvt_pk_fp8_f32 v197, v81, v85
	v_cvt_pk_fp8_f32 v197, v89, v93 op_sel:[0,0,1]
	v_cvt_pk_fp8_f32 v198, v97, v101
	v_cvt_pk_fp8_f32 v198, v105, v109 op_sel:[0,0,1]
	v_cvt_pk_fp8_f32 v199, v113, v117
	v_cvt_pk_fp8_f32 v199, v121, v125 op_sel:[0,0,1]
	global_store_dwordx4 v209, v[196:199], s[24:25] offset:2048 sc1
	v_cvt_pk_fp8_f32 v200, v66, v70
	v_cvt_pk_fp8_f32 v200, v74, v78 op_sel:[0,0,1]
	v_cvt_pk_fp8_f32 v201, v82, v86
	v_cvt_pk_fp8_f32 v201, v90, v94 op_sel:[0,0,1]
	v_cvt_pk_fp8_f32 v202, v98, v102
	v_cvt_pk_fp8_f32 v202, v106, v110 op_sel:[0,0,1]
	v_cvt_pk_fp8_f32 v203, v114, v118
	v_cvt_pk_fp8_f32 v203, v122, v126 op_sel:[0,0,1]
	global_store_dwordx4 v209, v[200:203], s[26:27] sc1
	v_cvt_pk_fp8_f32 v204, v67, v71
	v_cvt_pk_fp8_f32 v204, v75, v79 op_sel:[0,0,1]
	v_cvt_pk_fp8_f32 v205, v83, v87
	v_cvt_pk_fp8_f32 v205, v91, v95 op_sel:[0,0,1]
	v_cvt_pk_fp8_f32 v206, v99, v103
	v_cvt_pk_fp8_f32 v206, v107, v111 op_sel:[0,0,1]
	v_cvt_pk_fp8_f32 v207, v115, v119
	v_cvt_pk_fp8_f32 v207, v123, v127 op_sel:[0,0,1]
	global_store_dwordx4 v209, v[204:207], s[26:27] offset:2048 sc1
	s_waitcnt vmcnt(24)
	s_add_i32 s1, s20, 14
	s_lshr_b32 s2, s1, 10
	s_and_b32 s4, s1, 0x3ff
	s_lshr_b32 s5, s4, 6
	s_and_b32 s4, s4, 63
	s_lshl_b32 s12, s2, 22
	s_lshl_b32 s13, s4, 16
	s_add_i32 s12, s12, s13
	s_lshl_b32 s13, s5, 7
	s_add_i32 s12, s12, s13
	s_add_u32 s24, s90, s12
	s_addc_u32 s25, s91, 0
	s_add_u32 s24, s24, 0x3b100000
	s_addc_u32 s25, s25, 0
	s_add_u32 s26, s24, 0x1000
	s_addc_u32 s27, s25, 0
	v_pk_mul_f32 v[128:129], v[128:129], s[16:17] op_sel_hi:[1,0]
	v_pk_mul_f32 v[130:131], v[130:131], s[16:17] op_sel_hi:[1,0]
	v_pk_mul_f32 v[132:133], v[132:133], s[16:17] op_sel_hi:[1,0]
	v_pk_mul_f32 v[134:135], v[134:135], s[16:17] op_sel_hi:[1,0]
	v_pk_mul_f32 v[136:137], v[136:137], s[16:17] op_sel_hi:[1,0]
	v_pk_mul_f32 v[138:139], v[138:139], s[16:17] op_sel_hi:[1,0]
	v_pk_mul_f32 v[140:141], v[140:141], s[16:17] op_sel_hi:[1,0]
	v_pk_mul_f32 v[142:143], v[142:143], s[16:17] op_sel_hi:[1,0]
	v_pk_mul_f32 v[144:145], v[144:145], s[16:17] op_sel_hi:[1,0]
	v_pk_mul_f32 v[146:147], v[146:147], s[16:17] op_sel_hi:[1,0]
	v_pk_mul_f32 v[148:149], v[148:149], s[16:17] op_sel_hi:[1,0]
	v_pk_mul_f32 v[150:151], v[150:151], s[16:17] op_sel_hi:[1,0]
	v_pk_mul_f32 v[152:153], v[152:153], s[16:17] op_sel_hi:[1,0]
	v_pk_mul_f32 v[154:155], v[154:155], s[16:17] op_sel_hi:[1,0]
	v_pk_mul_f32 v[156:157], v[156:157], s[16:17] op_sel_hi:[1,0]
	v_pk_mul_f32 v[158:159], v[158:159], s[16:17] op_sel_hi:[1,0]
	v_pk_mul_f32 v[160:161], v[160:161], s[16:17] op_sel_hi:[1,0]
	v_pk_mul_f32 v[162:163], v[162:163], s[16:17] op_sel_hi:[1,0]
	v_pk_mul_f32 v[164:165], v[164:165], s[16:17] op_sel_hi:[1,0]
	v_pk_mul_f32 v[166:167], v[166:167], s[16:17] op_sel_hi:[1,0]
	v_pk_mul_f32 v[168:169], v[168:169], s[16:17] op_sel_hi:[1,0]
	v_pk_mul_f32 v[170:171], v[170:171], s[16:17] op_sel_hi:[1,0]
	v_pk_mul_f32 v[172:173], v[172:173], s[16:17] op_sel_hi:[1,0]
	v_pk_mul_f32 v[174:175], v[174:175], s[16:17] op_sel_hi:[1,0]
	v_pk_mul_f32 v[176:177], v[176:177], s[16:17] op_sel_hi:[1,0]
	v_pk_mul_f32 v[178:179], v[178:179], s[16:17] op_sel_hi:[1,0]
	v_pk_mul_f32 v[180:181], v[180:181], s[16:17] op_sel_hi:[1,0]
	v_pk_mul_f32 v[182:183], v[182:183], s[16:17] op_sel_hi:[1,0]
	v_pk_mul_f32 v[184:185], v[184:185], s[16:17] op_sel_hi:[1,0]
	v_pk_mul_f32 v[186:187], v[186:187], s[16:17] op_sel_hi:[1,0]
	v_pk_mul_f32 v[188:189], v[188:189], s[16:17] op_sel_hi:[1,0]
	v_pk_mul_f32 v[190:191], v[190:191], s[16:17] op_sel_hi:[1,0]
	v_cvt_pk_fp8_f32 v192, v128, v132
	v_cvt_pk_fp8_f32 v192, v136, v140 op_sel:[0,0,1]
	v_cvt_pk_fp8_f32 v193, v144, v148
	v_cvt_pk_fp8_f32 v193, v152, v156 op_sel:[0,0,1]
	v_cvt_pk_fp8_f32 v194, v160, v164
	v_cvt_pk_fp8_f32 v194, v168, v172 op_sel:[0,0,1]
	v_cvt_pk_fp8_f32 v195, v176, v180
	v_cvt_pk_fp8_f32 v195, v184, v188 op_sel:[0,0,1]
	global_store_dwordx4 v209, v[192:195], s[24:25] sc1
	v_cvt_pk_fp8_f32 v196, v129, v133
	v_cvt_pk_fp8_f32 v196, v137, v141 op_sel:[0,0,1]
	v_cvt_pk_fp8_f32 v197, v145, v149
	v_cvt_pk_fp8_f32 v197, v153, v157 op_sel:[0,0,1]
	v_cvt_pk_fp8_f32 v198, v161, v165
	v_cvt_pk_fp8_f32 v198, v169, v173 op_sel:[0,0,1]
	v_cvt_pk_fp8_f32 v199, v177, v181
	v_cvt_pk_fp8_f32 v199, v185, v189 op_sel:[0,0,1]
	global_store_dwordx4 v209, v[196:199], s[24:25] offset:2048 sc1
	v_cvt_pk_fp8_f32 v200, v130, v134
	v_cvt_pk_fp8_f32 v200, v138, v142 op_sel:[0,0,1]
	v_cvt_pk_fp8_f32 v201, v146, v150
	v_cvt_pk_fp8_f32 v201, v154, v158 op_sel:[0,0,1]
	v_cvt_pk_fp8_f32 v202, v162, v166
	v_cvt_pk_fp8_f32 v202, v170, v174 op_sel:[0,0,1]
	v_cvt_pk_fp8_f32 v203, v178, v182
	v_cvt_pk_fp8_f32 v203, v186, v190 op_sel:[0,0,1]
	global_store_dwordx4 v209, v[200:203], s[26:27] sc1
	v_cvt_pk_fp8_f32 v204, v131, v135
	v_cvt_pk_fp8_f32 v204, v139, v143 op_sel:[0,0,1]
	v_cvt_pk_fp8_f32 v205, v147, v151
	v_cvt_pk_fp8_f32 v205, v155, v159 op_sel:[0,0,1]
	v_cvt_pk_fp8_f32 v206, v163, v167
	v_cvt_pk_fp8_f32 v206, v171, v175 op_sel:[0,0,1]
	v_cvt_pk_fp8_f32 v207, v179, v183
	v_cvt_pk_fp8_f32 v207, v187, v191 op_sel:[0,0,1]
	global_store_dwordx4 v209, v[204:207], s[26:27] offset:2048 sc1
	s_waitcnt vmcnt(8)
	s_add_i32 s1, s20, 270
	s_lshr_b32 s2, s1, 10
	s_and_b32 s4, s1, 0x3ff
	s_lshr_b32 s5, s4, 6
	s_and_b32 s4, s4, 63
	s_lshl_b32 s12, s2, 22
	s_lshl_b32 s13, s4, 16
	s_add_i32 s12, s12, s13
	s_lshl_b32 s13, s5, 7
	s_add_i32 s12, s12, s13
	s_add_u32 s24, s90, s12
	s_addc_u32 s25, s91, 0
	s_add_u32 s24, s24, 0x3b100000
	s_addc_u32 s25, s25, 0
	s_add_u32 s26, s24, 0x1000
	s_addc_u32 s27, s25, 0
	v_pk_mul_f32 v[0:1], v[0:1], s[16:17] op_sel_hi:[1,0]
	v_pk_mul_f32 v[2:3], v[2:3], s[16:17] op_sel_hi:[1,0]
	v_pk_mul_f32 v[4:5], v[4:5], s[16:17] op_sel_hi:[1,0]
	v_pk_mul_f32 v[6:7], v[6:7], s[16:17] op_sel_hi:[1,0]
	v_pk_mul_f32 v[8:9], v[8:9], s[16:17] op_sel_hi:[1,0]
	v_pk_mul_f32 v[10:11], v[10:11], s[16:17] op_sel_hi:[1,0]
	v_pk_mul_f32 v[12:13], v[12:13], s[16:17] op_sel_hi:[1,0]
	v_pk_mul_f32 v[14:15], v[14:15], s[16:17] op_sel_hi:[1,0]
	v_pk_mul_f32 v[16:17], v[16:17], s[16:17] op_sel_hi:[1,0]
	v_pk_mul_f32 v[18:19], v[18:19], s[16:17] op_sel_hi:[1,0]
	v_pk_mul_f32 v[20:21], v[20:21], s[16:17] op_sel_hi:[1,0]
	v_pk_mul_f32 v[22:23], v[22:23], s[16:17] op_sel_hi:[1,0]
	v_pk_mul_f32 v[24:25], v[24:25], s[16:17] op_sel_hi:[1,0]
	v_pk_mul_f32 v[26:27], v[26:27], s[16:17] op_sel_hi:[1,0]
	v_pk_mul_f32 v[28:29], v[28:29], s[16:17] op_sel_hi:[1,0]
	v_pk_mul_f32 v[30:31], v[30:31], s[16:17] op_sel_hi:[1,0]
	v_pk_mul_f32 v[32:33], v[32:33], s[16:17] op_sel_hi:[1,0]
	v_pk_mul_f32 v[34:35], v[34:35], s[16:17] op_sel_hi:[1,0]
	v_pk_mul_f32 v[36:37], v[36:37], s[16:17] op_sel_hi:[1,0]
	v_pk_mul_f32 v[38:39], v[38:39], s[16:17] op_sel_hi:[1,0]
	v_pk_mul_f32 v[40:41], v[40:41], s[16:17] op_sel_hi:[1,0]
	v_pk_mul_f32 v[42:43], v[42:43], s[16:17] op_sel_hi:[1,0]
	v_pk_mul_f32 v[44:45], v[44:45], s[16:17] op_sel_hi:[1,0]
	v_pk_mul_f32 v[46:47], v[46:47], s[16:17] op_sel_hi:[1,0]
	v_pk_mul_f32 v[48:49], v[48:49], s[16:17] op_sel_hi:[1,0]
	v_pk_mul_f32 v[50:51], v[50:51], s[16:17] op_sel_hi:[1,0]
	v_pk_mul_f32 v[52:53], v[52:53], s[16:17] op_sel_hi:[1,0]
	v_pk_mul_f32 v[54:55], v[54:55], s[16:17] op_sel_hi:[1,0]
	v_pk_mul_f32 v[56:57], v[56:57], s[16:17] op_sel_hi:[1,0]
	v_pk_mul_f32 v[58:59], v[58:59], s[16:17] op_sel_hi:[1,0]
	v_pk_mul_f32 v[60:61], v[60:61], s[16:17] op_sel_hi:[1,0]
	v_pk_mul_f32 v[62:63], v[62:63], s[16:17] op_sel_hi:[1,0]
	v_cvt_pk_fp8_f32 v192, v0, v4
	v_cvt_pk_fp8_f32 v192, v8, v12 op_sel:[0,0,1]
	v_cvt_pk_fp8_f32 v193, v16, v20
	v_cvt_pk_fp8_f32 v193, v24, v28 op_sel:[0,0,1]
	v_cvt_pk_fp8_f32 v194, v32, v36
	v_cvt_pk_fp8_f32 v194, v40, v44 op_sel:[0,0,1]
	v_cvt_pk_fp8_f32 v195, v48, v52
	v_cvt_pk_fp8_f32 v195, v56, v60 op_sel:[0,0,1]
	global_store_dwordx4 v209, v[192:195], s[24:25] sc1
	v_cvt_pk_fp8_f32 v196, v1, v5
	v_cvt_pk_fp8_f32 v196, v9, v13 op_sel:[0,0,1]
	v_cvt_pk_fp8_f32 v197, v17, v21
	v_cvt_pk_fp8_f32 v197, v25, v29 op_sel:[0,0,1]
	v_cvt_pk_fp8_f32 v198, v33, v37
	v_cvt_pk_fp8_f32 v198, v41, v45 op_sel:[0,0,1]
	v_cvt_pk_fp8_f32 v199, v49, v53
	v_cvt_pk_fp8_f32 v199, v57, v61 op_sel:[0,0,1]
	global_store_dwordx4 v209, v[196:199], s[24:25] offset:2048 sc1
	v_cvt_pk_fp8_f32 v200, v2, v6
	v_cvt_pk_fp8_f32 v200, v10, v14 op_sel:[0,0,1]
	v_cvt_pk_fp8_f32 v201, v18, v22
	v_cvt_pk_fp8_f32 v201, v26, v30 op_sel:[0,0,1]
	v_cvt_pk_fp8_f32 v202, v34, v38
	v_cvt_pk_fp8_f32 v202, v42, v46 op_sel:[0,0,1]
	v_cvt_pk_fp8_f32 v203, v50, v54
	v_cvt_pk_fp8_f32 v203, v58, v62 op_sel:[0,0,1]
	global_store_dwordx4 v209, v[200:203], s[26:27] sc1
	v_cvt_pk_fp8_f32 v204, v3, v7
	v_cvt_pk_fp8_f32 v204, v11, v15 op_sel:[0,0,1]
	v_cvt_pk_fp8_f32 v205, v19, v23
	v_cvt_pk_fp8_f32 v205, v27, v31 op_sel:[0,0,1]
	v_cvt_pk_fp8_f32 v206, v35, v39
	v_cvt_pk_fp8_f32 v206, v43, v47 op_sel:[0,0,1]
	v_cvt_pk_fp8_f32 v207, v51, v55
	v_cvt_pk_fp8_f32 v207, v59, v63 op_sel:[0,0,1]
	global_store_dwordx4 v209, v[204:207], s[26:27] offset:2048 sc1
	s_waitcnt vmcnt(0)
	v_readlane_b32 s3, v255, 4
